# attention and retention-output task epilogues: per-lane 8-byte row stores staged through a per-wave LDS tile and written as lane-contiguous 16-byte stores
# speedup vs baseline: 1.0275x; 1.0034x over previous
; __device__ __forceinline__ float rq_sum(float v) { v += __shfl_xor(v, 16); v += __shfl_xor(v, 32); return v; }
; __device__ __forceinline__ float frsq(float x) { return __builtin_amdgcn_rsqf(x); }
; __device__ __forceinline__ void attn_wg_task(const Frame& F, int l, int task) {
;     ...
;     for (int qb = 0; qb < 2; ++qb) {
;         const int tq = tq0 + qb * 16;
;         const float inv = 1.0f / rq_sum(l_run[qb]);
;         float ss = 0.f;
; #pragma unroll
;         for (int db = 0; db < 8; ++db) { O[qb][db] *= inv; ss += (O[qb][db][0] * O[qb][db][0] + O[qb][db][1] * O[qb][db][1]) + (O[qb][db][2] * O[qb][db][2] + O[qb][db][3] * O[qb][db][3]); }
;         const float rstd = frsq(rq_sum(ss) * (1.f / HD) + EPS);
; #pragma unroll
;         for (int db = 0; db < 8; ++db) {
;             const int d0 = h * HD + db * 16 + rq * 4;
;             const f32x4 g4 = ld_f4(F.attn_g + l * 1024 + d0);
.LBB0_517:
	ds_bpermute_b32 v64, v202, v151
	v_lshl_or_b32 v82, v204, 2, s17
	v_readlane_b32 s2, v251, 53
	v_readlane_b32 s3, v251, 54
	s_waitcnt lgkmcnt(0)
	v_add_f32_e32 v64, v151, v64
	ds_bpermute_b32 v65, v203, v64
	s_barrier
	s_waitcnt lgkmcnt(0)
	v_lshlrev_b32_e32 v184, 1, v82
	v_readlane_b32 s4, v253, 59
	v_add_f32_e32 v64, v64, v65
	v_div_scale_f32 v65, s[0:1], v64, v64, 1.0
	v_rcp_f32_e32 v66, v65
	v_readlane_b32 s5, v253, 60
	v_fma_f32 v67, -v65, v66, 1.0
	v_fmac_f32_e32 v66, v67, v66
	v_div_scale_f32 v67, vcc, 1.0, v64, 1.0
	v_mul_f32_e32 v68, v67, v66
	v_fma_f32 v69, -v65, v68, v67
	v_fmac_f32_e32 v68, v69, v66
	v_fma_f32 v65, -v65, v68, v67
	v_div_fmas_f32 v65, v65, v66, v68
	v_div_fixup_f32 v84, v65, v64, 1.0
	v_pk_mul_f32 v[80:81], v[32:33], v[84:85] op_sel_hi:[1,0]
	v_pk_mul_f32 v[76:77], v[36:37], v[84:85] op_sel_hi:[1,0]
	v_pk_mul_f32 v[78:79], v[34:35], v[84:85] op_sel_hi:[1,0]
	v_pk_mul_f32 v[74:75], v[38:39], v[84:85] op_sel_hi:[1,0]
	v_mov_b32_e32 v34, v81
	v_mov_b32_e32 v35, v77
	v_mov_b32_e32 v32, v80
	v_mov_b32_e32 v33, v76
	v_pk_mul_f32 v[34:35], v[34:35], v[34:35]
	v_mov_b32_e32 v36, v79
	v_mov_b32_e32 v37, v75
	v_pk_fma_f32 v[32:33], v[32:33], v[32:33], v[34:35]
	v_mov_b32_e32 v34, v78
	v_mov_b32_e32 v35, v74
	v_pk_mul_f32 v[36:37], v[36:37], v[36:37]
	v_pk_mul_f32 v[72:73], v[40:41], v[84:85] op_sel_hi:[1,0]
	v_pk_fma_f32 v[34:35], v[34:35], v[34:35], v[36:37]
	v_pk_mul_f32 v[70:71], v[42:43], v[84:85] op_sel_hi:[1,0]
	v_pk_add_f32 v[32:33], v[32:33], v[34:35]
	v_pk_mul_f32 v[34:35], v[70:71], v[70:71]
	v_pk_add_f32 v[32:33], v[32:33], v[32:33] op_sel_hi:[0,1]
	v_pk_mul_f32 v[36:37], v[72:73], v[72:73]
	v_pk_mul_f32 v[68:69], v[44:45], v[84:85] op_sel_hi:[1,0]
	v_pk_mov_b32 v[38:39], v[36:37], v[34:35] op_sel:[1,0]
	v_mov_b32_e32 v37, v35
	v_pk_mul_f32 v[66:67], v[46:47], v[84:85] op_sel_hi:[1,0]
	v_mul_f32_e32 v32, v68, v68
	v_pk_add_f32 v[34:35], v[38:39], v[36:37]
	v_pk_fma_f32 v[36:37], v[68:69], v[68:69], v[32:33] op_sel_hi:[1,1,0]
	v_mul_f32_e32 v32, v66, v66
	v_pk_add_f32 v[34:35], v[34:35], v[34:35] op_sel_hi:[0,1]
	v_pk_fma_f32 v[38:39], v[66:67], v[66:67], v[32:33] op_sel_hi:[1,1,0]
	v_pk_mul_f32 v[50:51], v[50:51], v[84:85] op_sel_hi:[1,0]
	v_pk_mul_f32 v[64:65], v[48:49], v[84:85] op_sel_hi:[1,0]
	v_mul_f32_e32 v34, v50, v50
	v_mul_f32_e32 v36, v64, v64
	v_mul_f32_e32 v38, v65, v65
	v_mul_f32_e32 v32, v51, v51
	v_pk_add_f32 v[36:37], v[36:37], v[38:39]
	v_pk_add_f32 v[32:33], v[34:35], v[32:33]
	v_pk_mul_f32 v[48:49], v[52:53], v[84:85] op_sel_hi:[1,0]
	v_pk_add_f32 v[32:33], v[36:37], v[32:33]
	v_pk_mul_f32 v[46:47], v[54:55], v[84:85] op_sel_hi:[1,0]
	v_pk_add_f32 v[32:33], v[32:33], v[32:33] op_sel_hi:[0,1]
	v_pk_mul_f32 v[34:35], v[46:47], v[46:47]
	v_pk_mul_f32 v[36:37], v[48:49], v[48:49]
	v_pk_mul_f32 v[44:45], v[56:57], v[84:85] op_sel_hi:[1,0]
	v_pk_mov_b32 v[38:39], v[36:37], v[34:35] op_sel:[1,0]
	v_mov_b32_e32 v37, v35
	v_pk_mul_f32 v[42:43], v[58:59], v[84:85] op_sel_hi:[1,0]
	v_mul_f32_e32 v32, v44, v44
	v_pk_add_f32 v[34:35], v[38:39], v[36:37]
	v_pk_fma_f32 v[40:41], v[44:45], v[44:45], v[32:33] op_sel_hi:[1,1,0]
	v_mul_f32_e32 v32, v42, v42
	v_pk_add_f32 v[34:35], v[34:35], v[34:35] op_sel_hi:[0,1]
	v_pk_fma_f32 v[52:53], v[42:43], v[42:43], v[32:33] op_sel_hi:[1,1,0]
	v_pk_mul_f32 v[36:37], v[62:63], v[84:85] op_sel_hi:[1,0]
	v_pk_mul_f32 v[38:39], v[60:61], v[84:85] op_sel_hi:[1,0]
	v_mul_f32_e32 v34, v36, v36
	v_mul_f32_e32 v40, v38, v38
	v_mul_f32_e32 v52, v39, v39
	v_mul_f32_e32 v32, v37, v37
	v_pk_add_f32 v[40:41], v[40:41], v[52:53]
	v_pk_add_f32 v[32:33], v[34:35], v[32:33]
	v_lshlrev_b32_e32 v54, 2, v82
	global_load_dwordx4 v[96:99], v54, s[42:43]
	global_load_dwordx4 v[100:103], v54, s[42:43] offset:64
	global_load_dwordx4 v[104:107], v54, s[42:43] offset:128
	global_load_dwordx4 v[108:111], v54, s[42:43] offset:192
	global_load_dwordx4 v[112:115], v54, s[42:43] offset:256
	global_load_dwordx4 v[116:119], v54, s[42:43] offset:320
	global_load_dwordx4 v[120:123], v54, s[42:43] offset:384
	global_load_dwordx4 v[124:127], v54, s[42:43] offset:448
	v_pk_add_f32 v[32:33], v[40:41], v[32:33]
	v_mov_b32_e32 v56, v80
	v_add_f32_e32 v32, v32, v33
	ds_bpermute_b32 v33, v202, v32
	v_mov_b32_e32 v57, v78
	v_mov_b32_e32 v78, v81
	s_waitcnt lgkmcnt(0)
	v_add_f32_e32 v32, v32, v33
	ds_bpermute_b32 v33, v203, v32
	s_waitcnt lgkmcnt(0)
	v_add_f32_e32 v32, v32, v33
	v_fmamk_f32 v32, v32, 0x3c000000, v214
	v_rsq_f32_e32 v40, v32
	v_lshlrev_b64 v[32:33], 12, v[152:153]
	v_lshl_add_u64 v[52:53], s[2:3], 0, v[32:33]
	s_waitcnt vmcnt(0)
; __device__ __forceinline__ unsigned pk2(float lo, float hi) { return f2bf(lo) | (f2bf(hi) << 16); }
; __device__ __forceinline__ void attn_wg_task(const Frame& F, int l, int task) {
;     ...
; #pragma unroll
;         for (int db = 0; db < 8; ++db) {
;             const int d0 = h * HD + db * 16 + rq * 4;
;             const f32x4 g4 = ld_f4(F.attn_g + l * 1024 + d0);
;             u32x2 o; o.x = pk2(O[qb][db][0] * rstd * g4[0], O[qb][db][1] * rstd * g4[1]); o.y = pk2(O[qb][db][2] * rstd * g4[2], O[qb][db][3] * rstd * g4[3]);
;             st_u2(MIX + (size_t)tq * D + d0, o);
	v_mov_b32_e32 v32, v96
	v_mov_b32_e32 v33, v97
	v_mov_b32_e32 v34, v98
	v_mov_b32_e32 v35, v99
	v_pk_mul_f32 v[56:57], v[56:57], v[40:41] op_sel_hi:[1,0]
	v_mov_b32_e32 v58, v32
	v_mov_b32_e32 v59, v34
	v_pk_mul_f32 v[56:57], v[58:59], v[56:57]
	v_pk_mul_f32 v[58:59], v[78:79], v[40:41] op_sel_hi:[1,0]
	v_mov_b32_e32 v34, v33
	v_pk_mul_f32 v[32:33], v[34:35], v[58:59]
	v_and_b32_sdwa v35, v56, v213 dst_sel:DWORD dst_unused:UNUSED_PAD src0_sel:WORD_1 src1_sel:DWORD
	v_add3_u32 v41, v56, v35, s76
	v_and_b32_sdwa v35, v33, v213 dst_sel:DWORD dst_unused:UNUSED_PAD src0_sel:WORD_1 src1_sel:DWORD
	v_and_b32_sdwa v55, v32, v213 dst_sel:DWORD dst_unused:UNUSED_PAD src0_sel:WORD_1 src1_sel:DWORD
	v_and_b32_sdwa v34, v57, v213 dst_sel:DWORD dst_unused:UNUSED_PAD src0_sel:WORD_1 src1_sel:DWORD
	v_add3_u32 v33, v33, v35, s76
	v_add3_u32 v32, v32, v55, s76
	v_add3_u32 v34, v57, v34, s76
	v_and_b32_e32 v33, 0xffff0000, v33
	v_and_b32_e32 v32, 0xffff0000, v32
	v_or_b32_sdwa v35, v33, v34 dst_sel:DWORD dst_unused:UNUSED_PAD src0_sel:DWORD src1_sel:WORD_1
	v_or_b32_sdwa v34, v32, v41 dst_sel:DWORD dst_unused:UNUSED_PAD src0_sel:DWORD src1_sel:WORD_1
	v_lshl_add_u64 v[32:33], v[52:53], 0, v[184:185]
	v_and_b32_e32 v128, 15, v211
	v_lshrrev_b32_e32 v129, 4, v211
	v_lshrrev_b32_e32 v134, 6, v212
	v_mul_u32_u24_e32 v134, 0x2200, v134
	v_add_u32_e32 v134, v229, v134
	v_lshlrev_b32_e32 v135, 3, v129
	v_sub_u32_e32 v132, v134, v135
	v_lshlrev_b32_e32 v135, 8, v129
	v_add_u32_e32 v133, v134, v135
	v_lshlrev_b32_e32 v135, 8, v128
	v_sub_u32_e32 v133, v133, v135
	v_mul_u32_u24_e32 v135, 0xff8, v129
	v_mul_u32_u24_e32 v136, 0xff0, v128
	v_sub_u32_e32 v136, v135, v136
	v_ashrrev_i32_e32 v137, 31, v136
	v_lshl_add_u64 v[130:131], v[32:33], 0, v[136:137]
	ds_write_b64 v132, v[34:35]
	v_mov_b32_e32 v56, v100
	v_mov_b32_e32 v57, v101
	v_mov_b32_e32 v58, v102
	v_mov_b32_e32 v59, v103
	v_mov_b32_e32 v34, v76
	v_mov_b32_e32 v35, v74
	v_pk_mul_f32 v[34:35], v[34:35], v[40:41] op_sel_hi:[1,0]
	v_mov_b32_e32 v74, v77
	v_mov_b32_e32 v52, v56
	v_mov_b32_e32 v53, v58
	v_pk_mul_f32 v[34:35], v[52:53], v[34:35]
	v_pk_mul_f32 v[52:53], v[74:75], v[40:41] op_sel_hi:[1,0]
	v_mov_b32_e32 v58, v57
	v_pk_mul_f32 v[52:53], v[58:59], v[52:53]
	v_and_b32_sdwa v41, v35, v213 dst_sel:DWORD dst_unused:UNUSED_PAD src0_sel:WORD_1 src1_sel:DWORD
	v_and_b32_sdwa v55, v34, v213 dst_sel:DWORD dst_unused:UNUSED_PAD src0_sel:WORD_1 src1_sel:DWORD
	v_add3_u32 v34, v34, v55, s76
	v_add3_u32 v35, v35, v41, s76
	v_and_b32_sdwa v41, v53, v213 dst_sel:DWORD dst_unused:UNUSED_PAD src0_sel:WORD_1 src1_sel:DWORD
	v_and_b32_sdwa v55, v52, v213 dst_sel:DWORD dst_unused:UNUSED_PAD src0_sel:WORD_1 src1_sel:DWORD
	v_add3_u32 v41, v53, v41, s76
	v_add3_u32 v52, v52, v55, s76
	v_and_b32_e32 v41, 0xffff0000, v41
	v_and_b32_e32 v52, 0xffff0000, v52
	v_or_b32_sdwa v35, v41, v35 dst_sel:DWORD dst_unused:UNUSED_PAD src0_sel:DWORD src1_sel:WORD_1
	v_or_b32_sdwa v34, v52, v34 dst_sel:DWORD dst_unused:UNUSED_PAD src0_sel:DWORD src1_sel:WORD_1
	ds_write_b64 v132, v[34:35] offset:32
	v_mov_b32_e32 v56, v104
	v_mov_b32_e32 v57, v105
	v_mov_b32_e32 v58, v106
	v_mov_b32_e32 v59, v107
	v_mov_b32_e32 v34, v72
	v_mov_b32_e32 v35, v70
	v_pk_mul_f32 v[34:35], v[34:35], v[40:41] op_sel_hi:[1,0]
	v_mov_b32_e32 v70, v73
	v_mov_b32_e32 v52, v56
	v_mov_b32_e32 v53, v58
	v_pk_mul_f32 v[34:35], v[52:53], v[34:35]
	v_pk_mul_f32 v[52:53], v[70:71], v[40:41] op_sel_hi:[1,0]
	v_mov_b32_e32 v58, v57
	v_pk_mul_f32 v[52:53], v[58:59], v[52:53]
	v_and_b32_sdwa v41, v35, v213 dst_sel:DWORD dst_unused:UNUSED_PAD src0_sel:WORD_1 src1_sel:DWORD
	v_and_b32_sdwa v55, v34, v213 dst_sel:DWORD dst_unused:UNUSED_PAD src0_sel:WORD_1 src1_sel:DWORD
	v_add3_u32 v34, v34, v55, s76
	v_add3_u32 v35, v35, v41, s76
	v_and_b32_sdwa v41, v53, v213 dst_sel:DWORD dst_unused:UNUSED_PAD src0_sel:WORD_1 src1_sel:DWORD
	v_and_b32_sdwa v55, v52, v213 dst_sel:DWORD dst_unused:UNUSED_PAD src0_sel:WORD_1 src1_sel:DWORD
	v_add3_u32 v41, v53, v41, s76
	v_add3_u32 v52, v52, v55, s76
	v_and_b32_e32 v41, 0xffff0000, v41
	v_and_b32_e32 v52, 0xffff0000, v52
	v_or_b32_sdwa v35, v41, v35 dst_sel:DWORD dst_unused:UNUSED_PAD src0_sel:DWORD src1_sel:WORD_1
	v_or_b32_sdwa v34, v52, v34 dst_sel:DWORD dst_unused:UNUSED_PAD src0_sel:DWORD src1_sel:WORD_1
	ds_write_b64 v132, v[34:35] offset:64
	v_mov_b32_e32 v56, v108
	v_mov_b32_e32 v57, v109
	v_mov_b32_e32 v58, v110
	v_mov_b32_e32 v59, v111
	v_mov_b32_e32 v34, v68
	v_mov_b32_e32 v35, v66
	v_pk_mul_f32 v[34:35], v[34:35], v[40:41] op_sel_hi:[1,0]
	v_mov_b32_e32 v66, v69
	v_mov_b32_e32 v52, v56
	v_mov_b32_e32 v53, v58
	v_pk_mul_f32 v[34:35], v[52:53], v[34:35]
	v_pk_mul_f32 v[52:53], v[66:67], v[40:41] op_sel_hi:[1,0]
	v_mov_b32_e32 v58, v57
	v_pk_mul_f32 v[52:53], v[58:59], v[52:53]
	v_and_b32_sdwa v41, v35, v213 dst_sel:DWORD dst_unused:UNUSED_PAD src0_sel:WORD_1 src1_sel:DWORD
	v_and_b32_sdwa v55, v34, v213 dst_sel:DWORD dst_unused:UNUSED_PAD src0_sel:WORD_1 src1_sel:DWORD
	v_add3_u32 v34, v34, v55, s76
	v_add3_u32 v35, v35, v41, s76
	v_and_b32_sdwa v41, v53, v213 dst_sel:DWORD dst_unused:UNUSED_PAD src0_sel:WORD_1 src1_sel:DWORD
	v_and_b32_sdwa v55, v52, v213 dst_sel:DWORD dst_unused:UNUSED_PAD src0_sel:WORD_1 src1_sel:DWORD
	v_add3_u32 v41, v53, v41, s76
	v_add3_u32 v52, v52, v55, s76
	v_and_b32_e32 v41, 0xffff0000, v41
	v_and_b32_e32 v52, 0xffff0000, v52
	v_or_b32_sdwa v35, v41, v35 dst_sel:DWORD dst_unused:UNUSED_PAD src0_sel:DWORD src1_sel:WORD_1
	v_or_b32_sdwa v34, v52, v34 dst_sel:DWORD dst_unused:UNUSED_PAD src0_sel:DWORD src1_sel:WORD_1
	ds_write_b64 v132, v[34:35] offset:96
	v_mov_b32_e32 v56, v112
	v_mov_b32_e32 v57, v113
; __device__ __forceinline__ unsigned pk2(float lo, float hi) { return f2bf(lo) | (f2bf(hi) << 16); }
; __device__ __forceinline__ void attn_wg_task(const Frame& F, int l, int task) {
;     ...
; #pragma unroll
;         for (int db = 0; db < 8; ++db) {
;             const int d0 = h * HD + db * 16 + rq * 4;
;             const f32x4 g4 = ld_f4(F.attn_g + l * 1024 + d0);
;             u32x2 o; o.x = pk2(O[qb][db][0] * rstd * g4[0], O[qb][db][1] * rstd * g4[1]); o.y = pk2(O[qb][db][2] * rstd * g4[2], O[qb][db][3] * rstd * g4[3]);
;             st_u2(MIX + (size_t)tq * D + d0, o);
	v_mov_b32_e32 v58, v114
	v_mov_b32_e32 v59, v115
	v_mov_b32_e32 v34, v64
	v_mov_b32_e32 v35, v50
	v_pk_mul_f32 v[34:35], v[34:35], v[40:41] op_sel_hi:[1,0]
	v_mov_b32_e32 v50, v65
	v_pk_mul_f32 v[50:51], v[50:51], v[40:41] op_sel_hi:[1,0]
	v_mov_b32_e32 v52, v56
	v_mov_b32_e32 v53, v58
	v_pk_mul_f32 v[34:35], v[52:53], v[34:35]
	v_mov_b32_e32 v58, v57
	v_pk_mul_f32 v[50:51], v[58:59], v[50:51]
	v_and_b32_sdwa v41, v35, v213 dst_sel:DWORD dst_unused:UNUSED_PAD src0_sel:WORD_1 src1_sel:DWORD
	v_and_b32_sdwa v52, v34, v213 dst_sel:DWORD dst_unused:UNUSED_PAD src0_sel:WORD_1 src1_sel:DWORD
	v_add3_u32 v34, v34, v52, s76
	v_add3_u32 v35, v35, v41, s76
	v_and_b32_sdwa v41, v51, v213 dst_sel:DWORD dst_unused:UNUSED_PAD src0_sel:WORD_1 src1_sel:DWORD
	v_and_b32_sdwa v52, v50, v213 dst_sel:DWORD dst_unused:UNUSED_PAD src0_sel:WORD_1 src1_sel:DWORD
	v_add3_u32 v41, v51, v41, s76
	v_add3_u32 v50, v50, v52, s76
	v_and_b32_e32 v41, 0xffff0000, v41
	v_and_b32_e32 v50, 0xffff0000, v50
	v_or_b32_sdwa v35, v41, v35 dst_sel:DWORD dst_unused:UNUSED_PAD src0_sel:DWORD src1_sel:WORD_1
	v_or_b32_sdwa v34, v50, v34 dst_sel:DWORD dst_unused:UNUSED_PAD src0_sel:DWORD src1_sel:WORD_1
	ds_write_b64 v132, v[34:35] offset:128
	v_mov_b32_e32 v50, v116
	v_mov_b32_e32 v51, v117
	v_mov_b32_e32 v52, v118
	v_mov_b32_e32 v53, v119
	v_mov_b32_e32 v34, v48
	v_mov_b32_e32 v35, v46
	v_pk_mul_f32 v[34:35], v[34:35], v[40:41] op_sel_hi:[1,0]
	v_mov_b32_e32 v46, v49
	v_pk_mul_f32 v[46:47], v[46:47], v[40:41] op_sel_hi:[1,0]
	v_mov_b32_e32 v56, v50
	v_mov_b32_e32 v57, v52
	v_pk_mul_f32 v[34:35], v[56:57], v[34:35]
	v_mov_b32_e32 v52, v51
	v_pk_mul_f32 v[46:47], v[52:53], v[46:47]
	v_and_b32_sdwa v41, v35, v213 dst_sel:DWORD dst_unused:UNUSED_PAD src0_sel:WORD_1 src1_sel:DWORD
	v_and_b32_sdwa v48, v34, v213 dst_sel:DWORD dst_unused:UNUSED_PAD src0_sel:WORD_1 src1_sel:DWORD
	v_add3_u32 v34, v34, v48, s76
	v_add3_u32 v35, v35, v41, s76
	v_and_b32_sdwa v41, v47, v213 dst_sel:DWORD dst_unused:UNUSED_PAD src0_sel:WORD_1 src1_sel:DWORD
	v_and_b32_sdwa v48, v46, v213 dst_sel:DWORD dst_unused:UNUSED_PAD src0_sel:WORD_1 src1_sel:DWORD
	v_add3_u32 v41, v47, v41, s76
	v_add3_u32 v46, v46, v48, s76
	v_and_b32_e32 v41, 0xffff0000, v41
	v_and_b32_e32 v46, 0xffff0000, v46
	v_or_b32_sdwa v35, v41, v35 dst_sel:DWORD dst_unused:UNUSED_PAD src0_sel:DWORD src1_sel:WORD_1
	v_or_b32_sdwa v34, v46, v34 dst_sel:DWORD dst_unused:UNUSED_PAD src0_sel:DWORD src1_sel:WORD_1
	ds_write_b64 v132, v[34:35] offset:160
	v_mov_b32_e32 v46, v120
	v_mov_b32_e32 v47, v121
	v_mov_b32_e32 v48, v122
	v_mov_b32_e32 v49, v123
	v_mov_b32_e32 v34, v44
	v_mov_b32_e32 v35, v42
	v_pk_mul_f32 v[34:35], v[34:35], v[40:41] op_sel_hi:[1,0]
	v_mov_b32_e32 v42, v45
	v_pk_mul_f32 v[42:43], v[42:43], v[40:41] op_sel_hi:[1,0]
	v_mov_b32_e32 v50, v46
	v_mov_b32_e32 v51, v48
	v_pk_mul_f32 v[34:35], v[50:51], v[34:35]
	v_mov_b32_e32 v48, v47
	v_pk_mul_f32 v[42:43], v[48:49], v[42:43]
	v_and_b32_sdwa v41, v35, v213 dst_sel:DWORD dst_unused:UNUSED_PAD src0_sel:WORD_1 src1_sel:DWORD
	v_and_b32_sdwa v44, v34, v213 dst_sel:DWORD dst_unused:UNUSED_PAD src0_sel:WORD_1 src1_sel:DWORD
	v_add3_u32 v34, v34, v44, s76
	v_add3_u32 v35, v35, v41, s76
	v_and_b32_sdwa v41, v43, v213 dst_sel:DWORD dst_unused:UNUSED_PAD src0_sel:WORD_1 src1_sel:DWORD
	v_and_b32_sdwa v44, v42, v213 dst_sel:DWORD dst_unused:UNUSED_PAD src0_sel:WORD_1 src1_sel:DWORD
	v_add3_u32 v41, v43, v41, s76
	v_add3_u32 v42, v42, v44, s76
	v_and_b32_e32 v41, 0xffff0000, v41
	v_and_b32_e32 v42, 0xffff0000, v42
	v_or_b32_sdwa v35, v41, v35 dst_sel:DWORD dst_unused:UNUSED_PAD src0_sel:DWORD src1_sel:WORD_1
	v_or_b32_sdwa v34, v42, v34 dst_sel:DWORD dst_unused:UNUSED_PAD src0_sel:DWORD src1_sel:WORD_1
	ds_write_b64 v132, v[34:35] offset:192
	v_mov_b32_e32 v42, v124
	v_mov_b32_e32 v43, v125
	v_mov_b32_e32 v44, v126
	v_mov_b32_e32 v45, v127
	v_mov_b32_e32 v34, v38
	v_mov_b32_e32 v35, v36
	v_pk_mul_f32 v[34:35], v[34:35], v[40:41] op_sel_hi:[1,0]
	v_mov_b32_e32 v36, v39
	v_pk_mul_f32 v[36:37], v[36:37], v[40:41] op_sel_hi:[1,0]
	v_mov_b32_e32 v46, v42
	v_mov_b32_e32 v47, v44
	v_pk_mul_f32 v[34:35], v[46:47], v[34:35]
	v_mov_b32_e32 v44, v43
	v_pk_mul_f32 v[36:37], v[44:45], v[36:37]
	v_and_b32_sdwa v38, v35, v213 dst_sel:DWORD dst_unused:UNUSED_PAD src0_sel:WORD_1 src1_sel:DWORD
	v_and_b32_sdwa v39, v34, v213 dst_sel:DWORD dst_unused:UNUSED_PAD src0_sel:WORD_1 src1_sel:DWORD
	v_add3_u32 v34, v34, v39, s76
	v_add3_u32 v35, v35, v38, s76
	v_and_b32_sdwa v38, v37, v213 dst_sel:DWORD dst_unused:UNUSED_PAD src0_sel:WORD_1 src1_sel:DWORD
	v_and_b32_sdwa v39, v36, v213 dst_sel:DWORD dst_unused:UNUSED_PAD src0_sel:WORD_1 src1_sel:DWORD
	v_add3_u32 v37, v37, v38, s76
	v_add3_u32 v36, v36, v39, s76
	v_and_b32_e32 v37, 0xffff0000, v37
	v_and_b32_e32 v36, 0xffff0000, v36
	v_or_b32_sdwa v35, v37, v35 dst_sel:DWORD dst_unused:UNUSED_PAD src0_sel:DWORD src1_sel:WORD_1
	v_or_b32_sdwa v34, v36, v34 dst_sel:DWORD dst_unused:UNUSED_PAD src0_sel:DWORD src1_sel:WORD_1
	ds_write_b64 v132, v[34:35] offset:224
	ds_bpermute_b32 v32, v202, v150
	s_waitcnt lgkmcnt(0)
	v_add_f32_e32 v32, v150, v32
	ds_bpermute_b32 v33, v203, v32
	s_waitcnt lgkmcnt(0)
; __device__ __forceinline__ unsigned pk2(float lo, float hi) { return f2bf(lo) | (f2bf(hi) << 16); }
; __device__ __forceinline__ float rq_sum(float v) { v += __shfl_xor(v, 16); v += __shfl_xor(v, 32); return v; }
; __device__ __forceinline__ float frsq(float x) { return __builtin_amdgcn_rsqf(x); }
; __device__ __forceinline__ void attn_wg_task(const Frame& F, int l, int task) {
;     ...
;     for (int qb = 0; qb < 2; ++qb) {
;         const int tq = tq0 + qb * 16;
;         const float inv = 1.0f / rq_sum(l_run[qb]);
;         float ss = 0.f;
; #pragma unroll
;         for (int db = 0; db < 8; ++db) { O[qb][db] *= inv; ss += (O[qb][db][0] * O[qb][db][0] + O[qb][db][1] * O[qb][db][1]) + (O[qb][db][2] * O[qb][db][2] + O[qb][db][3] * O[qb][db][3]); }
;         const float rstd = frsq(rq_sum(ss) * (1.f / HD) + EPS);
; #pragma unroll
;         for (int db = 0; db < 8; ++db) {
;             const int d0 = h * HD + db * 16 + rq * 4;
;             const f32x4 g4 = ld_f4(F.attn_g + l * 1024 + d0);
;             u32x2 o; o.x = pk2(O[qb][db][0] * rstd * g4[0], O[qb][db][1] * rstd * g4[1]); o.y = pk2(O[qb][db][2] * rstd * g4[2], O[qb][db][3] * rstd * g4[3]);
;             st_u2(MIX + (size_t)tq * D + d0, o);
	v_add_f32_e32 v32, v32, v33
	v_div_scale_f32 v33, s[0:1], v32, v32, 1.0
	v_rcp_f32_e32 v34, v33
	s_nop 0
	v_fma_f32 v35, -v33, v34, 1.0
	v_fmac_f32_e32 v34, v35, v34
	v_div_scale_f32 v35, vcc, 1.0, v32, 1.0
	v_mul_f32_e32 v36, v35, v34
	v_fma_f32 v37, -v33, v36, v35
	v_fmac_f32_e32 v36, v37, v34
	v_fma_f32 v33, -v33, v36, v35
	v_div_fmas_f32 v33, v33, v34, v36
	v_div_fixup_f32 v48, v33, v32, 1.0
	v_pk_mul_f32 v[46:47], v[4:5], v[48:49] op_sel_hi:[1,0]
	v_pk_mul_f32 v[42:43], v[8:9], v[48:49] op_sel_hi:[1,0]
	v_pk_mul_f32 v[44:45], v[6:7], v[48:49] op_sel_hi:[1,0]
	v_pk_mul_f32 v[36:37], v[10:11], v[48:49] op_sel_hi:[1,0]
	v_mov_b32_e32 v6, v47
	v_mov_b32_e32 v7, v43
	v_mov_b32_e32 v4, v46
	v_mov_b32_e32 v5, v42
	v_pk_mul_f32 v[6:7], v[6:7], v[6:7]
	v_mov_b32_e32 v8, v45
	v_mov_b32_e32 v9, v37
	v_pk_fma_f32 v[4:5], v[4:5], v[4:5], v[6:7]
	v_mov_b32_e32 v6, v44
	v_mov_b32_e32 v7, v36
	v_pk_mul_f32 v[8:9], v[8:9], v[8:9]
	v_pk_mul_f32 v[40:41], v[0:1], v[48:49] op_sel_hi:[1,0]
	v_pk_mul_f32 v[38:39], v[2:3], v[48:49] op_sel_hi:[1,0]
	v_pk_fma_f32 v[6:7], v[6:7], v[6:7], v[8:9]
	v_pk_mul_f32 v[0:1], v[38:39], v[38:39]
	v_pk_mul_f32 v[2:3], v[40:41], v[40:41]
	v_pk_add_f32 v[4:5], v[4:5], v[6:7]
	v_pk_mov_b32 v[6:7], v[2:3], v[0:1] op_sel:[1,0]
	v_mov_b32_e32 v3, v1
	v_pk_add_f32 v[0:1], v[6:7], v[2:3]
	v_pk_mul_f32 v[34:35], v[12:13], v[48:49] op_sel_hi:[1,0]
	v_pk_add_f32 v[0:1], v[0:1], v[0:1] op_sel_hi:[0,1]
	v_pk_mul_f32 v[32:33], v[14:15], v[48:49] op_sel_hi:[1,0]
	v_mul_f32_e32 v0, v34, v34
	v_pk_fma_f32 v[2:3], v[34:35], v[34:35], v[0:1] op_sel_hi:[1,1,0]
	v_mul_f32_e32 v0, v32, v32
	v_pk_add_f32 v[4:5], v[4:5], v[4:5] op_sel_hi:[0,1]
	v_pk_fma_f32 v[6:7], v[32:33], v[32:33], v[0:1] op_sel_hi:[1,1,0]
	v_pk_mul_f32 v[14:15], v[18:19], v[48:49] op_sel_hi:[1,0]
	v_pk_mul_f32 v[16:17], v[16:17], v[48:49] op_sel_hi:[1,0]
	v_mul_f32_e32 v0, v14, v14
	v_mul_f32_e32 v2, v16, v16
	v_mul_f32_e32 v6, v17, v17
	v_mul_f32_e32 v4, v15, v15
	v_pk_add_f32 v[2:3], v[2:3], v[6:7]
	v_pk_add_f32 v[0:1], v[0:1], v[4:5]
	v_pk_mul_f32 v[12:13], v[20:21], v[48:49] op_sel_hi:[1,0]
	v_pk_add_f32 v[0:1], v[2:3], v[0:1]
	v_pk_mul_f32 v[10:11], v[22:23], v[48:49] op_sel_hi:[1,0]
	v_pk_add_f32 v[4:5], v[0:1], v[0:1] op_sel_hi:[0,1]
	v_pk_mul_f32 v[0:1], v[10:11], v[10:11]
	v_pk_mul_f32 v[2:3], v[12:13], v[12:13]
	v_pk_mul_f32 v[8:9], v[24:25], v[48:49] op_sel_hi:[1,0]
	v_pk_mov_b32 v[6:7], v[2:3], v[0:1] op_sel:[1,0]
	v_mov_b32_e32 v3, v1
	v_pk_add_f32 v[0:1], v[6:7], v[2:3]
	v_pk_mul_f32 v[6:7], v[26:27], v[48:49] op_sel_hi:[1,0]
	v_pk_add_f32 v[18:19], v[0:1], v[0:1] op_sel_hi:[0,1]
	v_mul_f32_e32 v0, v8, v8
	v_pk_fma_f32 v[20:21], v[8:9], v[8:9], v[0:1] op_sel_hi:[1,1,0]
	v_mul_f32_e32 v0, v6, v6
	v_pk_fma_f32 v[22:23], v[6:7], v[6:7], v[0:1] op_sel_hi:[1,1,0]
	v_pk_mul_f32 v[0:1], v[30:31], v[48:49] op_sel_hi:[1,0]
	v_pk_mul_f32 v[2:3], v[28:29], v[48:49] op_sel_hi:[1,0]
	v_mul_f32_e32 v18, v0, v0
	v_mul_f32_e32 v20, v2, v2
	v_mul_f32_e32 v22, v3, v3
	v_mul_f32_e32 v4, v1, v1
	v_pk_add_f32 v[20:21], v[20:21], v[22:23]
	v_pk_add_f32 v[4:5], v[18:19], v[4:5]
	v_mov_b32_e32 v24, v46
	v_pk_add_f32 v[4:5], v[20:21], v[4:5]
	v_mov_b32_e32 v20, v96
	v_mov_b32_e32 v21, v97
	v_mov_b32_e32 v22, v98
	v_mov_b32_e32 v23, v99
	v_add_f32_e32 v4, v4, v5
	ds_bpermute_b32 v5, v202, v4
	v_mov_b32_e32 v25, v44
	v_mov_b32_e32 v44, v47
	v_lshlrev_b64 v[18:19], 12, v[148:149]
	v_lshl_add_u64 v[18:19], s[2:3], 0, v[18:19]
	s_waitcnt lgkmcnt(0)
	v_add_f32_e32 v4, v4, v5
	ds_bpermute_b32 v5, v203, v4
	v_lshl_add_u64 v[18:19], v[18:19], 0, v[184:185]
	s_add_i32 s2, s16, 1
	s_cmp_lt_u32 s16, 2
	s_cselect_b64 s[0:1], -1, 0
	s_waitcnt lgkmcnt(0)
	v_add_f32_e32 v4, v4, v5
	v_fmamk_f32 v4, v4, 0x3c000000, v214
	v_rsq_f32_e32 v4, v4
	s_and_b64 s[0:1], s[4:5], s[0:1]
	s_andn2_b64 vcc, exec, s[0:1]
	s_mov_b32 s16, s2
	v_pk_mul_f32 v[24:25], v[24:25], v[4:5] op_sel_hi:[1,0]
	v_mov_b32_e32 v26, v20
	v_mov_b32_e32 v27, v22
	v_pk_mul_f32 v[24:25], v[26:27], v[24:25]
	v_pk_mul_f32 v[26:27], v[44:45], v[4:5] op_sel_hi:[1,0]
	v_mov_b32_e32 v22, v21
	v_pk_mul_f32 v[20:21], v[22:23], v[26:27]
	v_and_b32_sdwa v22, v24, v213 dst_sel:DWORD dst_unused:UNUSED_PAD src0_sel:WORD_1 src1_sel:DWORD
	v_add3_u32 v22, v24, v22, s76
	v_and_b32_sdwa v23, v21, v213 dst_sel:DWORD dst_unused:UNUSED_PAD src0_sel:WORD_1 src1_sel:DWORD
	v_and_b32_sdwa v24, v20, v213 dst_sel:DWORD dst_unused:UNUSED_PAD src0_sel:WORD_1 src1_sel:DWORD
	v_and_b32_sdwa v5, v25, v213 dst_sel:DWORD dst_unused:UNUSED_PAD src0_sel:WORD_1 src1_sel:DWORD
	v_add3_u32 v21, v21, v23, s76
	v_add3_u32 v20, v20, v24, s76
	v_add3_u32 v5, v25, v5, s76
	v_and_b32_e32 v21, 0xffff0000, v21
	v_and_b32_e32 v20, 0xffff0000, v20
	v_or_b32_sdwa v21, v21, v5 dst_sel:DWORD dst_unused:UNUSED_PAD src0_sel:DWORD src1_sel:WORD_1
	v_or_b32_sdwa v20, v20, v22 dst_sel:DWORD dst_unused:UNUSED_PAD src0_sel:DWORD src1_sel:WORD_1
	ds_write_b64 v132, v[20:21] offset:4352
	v_mov_b32_e32 v20, v100
	v_mov_b32_e32 v21, v101
	v_mov_b32_e32 v22, v102
	v_mov_b32_e32 v23, v103
	v_mov_b32_e32 v24, v42
	v_mov_b32_e32 v25, v36
	v_pk_mul_f32 v[24:25], v[24:25], v[4:5] op_sel_hi:[1,0]
	v_mov_b32_e32 v36, v43
	v_mov_b32_e32 v26, v20
	v_mov_b32_e32 v27, v22
	v_pk_mul_f32 v[24:25], v[26:27], v[24:25]
	v_pk_mul_f32 v[26:27], v[36:37], v[4:5] op_sel_hi:[1,0]
	v_mov_b32_e32 v22, v21
	v_pk_mul_f32 v[20:21], v[22:23], v[26:27]
	v_and_b32_sdwa v22, v24, v213 dst_sel:DWORD dst_unused:UNUSED_PAD src0_sel:WORD_1 src1_sel:DWORD
	v_add3_u32 v22, v24, v22, s76
	v_and_b32_sdwa v23, v21, v213 dst_sel:DWORD dst_unused:UNUSED_PAD src0_sel:WORD_1 src1_sel:DWORD
; __device__ __forceinline__ unsigned pk2(float lo, float hi) { return f2bf(lo) | (f2bf(hi) << 16); }
; __device__ __forceinline__ void attn_wg_task(const Frame& F, int l, int task) {
;     ...
; #pragma unroll
;         for (int db = 0; db < 8; ++db) {
;             const int d0 = h * HD + db * 16 + rq * 4;
;             const f32x4 g4 = ld_f4(F.attn_g + l * 1024 + d0);
;             u32x2 o; o.x = pk2(O[qb][db][0] * rstd * g4[0], O[qb][db][1] * rstd * g4[1]); o.y = pk2(O[qb][db][2] * rstd * g4[2], O[qb][db][3] * rstd * g4[3]);
;             st_u2(MIX + (size_t)tq * D + d0, o);
	v_and_b32_sdwa v24, v20, v213 dst_sel:DWORD dst_unused:UNUSED_PAD src0_sel:WORD_1 src1_sel:DWORD
	v_and_b32_sdwa v5, v25, v213 dst_sel:DWORD dst_unused:UNUSED_PAD src0_sel:WORD_1 src1_sel:DWORD
	v_add3_u32 v21, v21, v23, s76
	v_add3_u32 v20, v20, v24, s76
	v_add3_u32 v5, v25, v5, s76
	v_and_b32_e32 v21, 0xffff0000, v21
	v_and_b32_e32 v20, 0xffff0000, v20
	v_or_b32_sdwa v21, v21, v5 dst_sel:DWORD dst_unused:UNUSED_PAD src0_sel:DWORD src1_sel:WORD_1
	v_or_b32_sdwa v20, v20, v22 dst_sel:DWORD dst_unused:UNUSED_PAD src0_sel:DWORD src1_sel:WORD_1
	ds_write_b64 v132, v[20:21] offset:4384
	v_mov_b32_e32 v20, v104
	v_mov_b32_e32 v21, v105
	v_mov_b32_e32 v22, v106
	v_mov_b32_e32 v23, v107
	v_mov_b32_e32 v24, v40
	v_mov_b32_e32 v25, v38
	v_pk_mul_f32 v[24:25], v[24:25], v[4:5] op_sel_hi:[1,0]
	v_mov_b32_e32 v38, v41
	v_mov_b32_e32 v26, v20
	v_mov_b32_e32 v27, v22
	v_pk_mul_f32 v[24:25], v[26:27], v[24:25]
	v_pk_mul_f32 v[26:27], v[38:39], v[4:5] op_sel_hi:[1,0]
	v_mov_b32_e32 v22, v21
	v_pk_mul_f32 v[20:21], v[22:23], v[26:27]
	v_and_b32_sdwa v22, v24, v213 dst_sel:DWORD dst_unused:UNUSED_PAD src0_sel:WORD_1 src1_sel:DWORD
	v_add3_u32 v22, v24, v22, s76
	v_and_b32_sdwa v23, v21, v213 dst_sel:DWORD dst_unused:UNUSED_PAD src0_sel:WORD_1 src1_sel:DWORD
	v_and_b32_sdwa v24, v20, v213 dst_sel:DWORD dst_unused:UNUSED_PAD src0_sel:WORD_1 src1_sel:DWORD
	v_and_b32_sdwa v5, v25, v213 dst_sel:DWORD dst_unused:UNUSED_PAD src0_sel:WORD_1 src1_sel:DWORD
	v_add3_u32 v21, v21, v23, s76
	v_add3_u32 v20, v20, v24, s76
	v_add3_u32 v5, v25, v5, s76
	v_and_b32_e32 v21, 0xffff0000, v21
	v_and_b32_e32 v20, 0xffff0000, v20
	v_or_b32_sdwa v21, v21, v5 dst_sel:DWORD dst_unused:UNUSED_PAD src0_sel:DWORD src1_sel:WORD_1
	v_or_b32_sdwa v20, v20, v22 dst_sel:DWORD dst_unused:UNUSED_PAD src0_sel:DWORD src1_sel:WORD_1
	ds_write_b64 v132, v[20:21] offset:4416
	v_mov_b32_e32 v20, v108
	v_mov_b32_e32 v21, v109
	v_mov_b32_e32 v22, v110
	v_mov_b32_e32 v23, v111
	v_mov_b32_e32 v24, v34
	v_mov_b32_e32 v25, v32
	v_pk_mul_f32 v[24:25], v[24:25], v[4:5] op_sel_hi:[1,0]
	v_mov_b32_e32 v32, v35
	v_mov_b32_e32 v26, v20
	v_mov_b32_e32 v27, v22
	v_pk_mul_f32 v[24:25], v[26:27], v[24:25]
	v_pk_mul_f32 v[26:27], v[32:33], v[4:5] op_sel_hi:[1,0]
	v_mov_b32_e32 v22, v21
	v_pk_mul_f32 v[20:21], v[22:23], v[26:27]
	v_and_b32_sdwa v22, v24, v213 dst_sel:DWORD dst_unused:UNUSED_PAD src0_sel:WORD_1 src1_sel:DWORD
	v_add3_u32 v22, v24, v22, s76
	v_and_b32_sdwa v23, v21, v213 dst_sel:DWORD dst_unused:UNUSED_PAD src0_sel:WORD_1 src1_sel:DWORD
	v_and_b32_sdwa v24, v20, v213 dst_sel:DWORD dst_unused:UNUSED_PAD src0_sel:WORD_1 src1_sel:DWORD
	v_and_b32_sdwa v5, v25, v213 dst_sel:DWORD dst_unused:UNUSED_PAD src0_sel:WORD_1 src1_sel:DWORD
	v_add3_u32 v21, v21, v23, s76
	v_add3_u32 v20, v20, v24, s76
	v_add3_u32 v5, v25, v5, s76
	v_and_b32_e32 v21, 0xffff0000, v21
	v_and_b32_e32 v20, 0xffff0000, v20
	v_or_b32_sdwa v21, v21, v5 dst_sel:DWORD dst_unused:UNUSED_PAD src0_sel:DWORD src1_sel:WORD_1
	v_or_b32_sdwa v20, v20, v22 dst_sel:DWORD dst_unused:UNUSED_PAD src0_sel:DWORD src1_sel:WORD_1
	ds_write_b64 v132, v[20:21] offset:4448
	v_mov_b32_e32 v20, v112
	v_mov_b32_e32 v21, v113
	v_mov_b32_e32 v22, v114
	v_mov_b32_e32 v23, v115
	v_mov_b32_e32 v25, v14
	v_mov_b32_e32 v14, v17
	v_mov_b32_e32 v24, v16
	v_pk_mul_f32 v[14:15], v[14:15], v[4:5] op_sel_hi:[1,0]
	v_pk_mul_f32 v[24:25], v[24:25], v[4:5] op_sel_hi:[1,0]
	v_mov_b32_e32 v27, v22
	v_mov_b32_e32 v22, v21
	v_mov_b32_e32 v26, v20
	v_pk_mul_f32 v[14:15], v[22:23], v[14:15]
	v_pk_mul_f32 v[24:25], v[26:27], v[24:25]
	v_and_b32_sdwa v17, v15, v213 dst_sel:DWORD dst_unused:UNUSED_PAD src0_sel:WORD_1 src1_sel:DWORD
	v_and_b32_sdwa v20, v14, v213 dst_sel:DWORD dst_unused:UNUSED_PAD src0_sel:WORD_1 src1_sel:DWORD
	v_and_b32_sdwa v5, v25, v213 dst_sel:DWORD dst_unused:UNUSED_PAD src0_sel:WORD_1 src1_sel:DWORD
	v_and_b32_sdwa v16, v24, v213 dst_sel:DWORD dst_unused:UNUSED_PAD src0_sel:WORD_1 src1_sel:DWORD
	v_add3_u32 v15, v15, v17, s76
	v_add3_u32 v14, v14, v20, s76
	v_add3_u32 v16, v24, v16, s76
	v_add3_u32 v5, v25, v5, s76
	v_and_b32_e32 v15, 0xffff0000, v15
	v_and_b32_e32 v14, 0xffff0000, v14
	v_or_b32_sdwa v15, v15, v5 dst_sel:DWORD dst_unused:UNUSED_PAD src0_sel:DWORD src1_sel:WORD_1
	v_or_b32_sdwa v14, v14, v16 dst_sel:DWORD dst_unused:UNUSED_PAD src0_sel:DWORD src1_sel:WORD_1
	ds_write_b64 v132, v[14:15] offset:4480
	v_mov_b32_e32 v14, v116
	v_mov_b32_e32 v15, v117
	v_mov_b32_e32 v16, v118
	v_mov_b32_e32 v17, v119
	v_mov_b32_e32 v21, v10
	v_mov_b32_e32 v10, v13
	v_mov_b32_e32 v20, v12
	v_pk_mul_f32 v[10:11], v[10:11], v[4:5] op_sel_hi:[1,0]
	v_pk_mul_f32 v[20:21], v[20:21], v[4:5] op_sel_hi:[1,0]
	v_mov_b32_e32 v23, v16
	v_mov_b32_e32 v16, v15
	v_mov_b32_e32 v22, v14
; __device__ __forceinline__ unsigned pk2(float lo, float hi) { return f2bf(lo) | (f2bf(hi) << 16); }
; __device__ __forceinline__ void attn_wg_task(const Frame& F, int l, int task) {
;     ...
; #pragma unroll
;         for (int db = 0; db < 8; ++db) {
;             const int d0 = h * HD + db * 16 + rq * 4;
;             const f32x4 g4 = ld_f4(F.attn_g + l * 1024 + d0);
;             u32x2 o; o.x = pk2(O[qb][db][0] * rstd * g4[0], O[qb][db][1] * rstd * g4[1]); o.y = pk2(O[qb][db][2] * rstd * g4[2], O[qb][db][3] * rstd * g4[3]);
;             st_u2(MIX + (size_t)tq * D + d0, o);
	v_pk_mul_f32 v[10:11], v[16:17], v[10:11]
	v_pk_mul_f32 v[20:21], v[22:23], v[20:21]
	v_and_b32_sdwa v13, v11, v213 dst_sel:DWORD dst_unused:UNUSED_PAD src0_sel:WORD_1 src1_sel:DWORD
	v_and_b32_sdwa v14, v10, v213 dst_sel:DWORD dst_unused:UNUSED_PAD src0_sel:WORD_1 src1_sel:DWORD
	v_and_b32_sdwa v5, v21, v213 dst_sel:DWORD dst_unused:UNUSED_PAD src0_sel:WORD_1 src1_sel:DWORD
	v_and_b32_sdwa v12, v20, v213 dst_sel:DWORD dst_unused:UNUSED_PAD src0_sel:WORD_1 src1_sel:DWORD
	v_add3_u32 v11, v11, v13, s76
	v_add3_u32 v10, v10, v14, s76
	v_add3_u32 v12, v20, v12, s76
	v_add3_u32 v5, v21, v5, s76
	v_and_b32_e32 v11, 0xffff0000, v11
	v_and_b32_e32 v10, 0xffff0000, v10
	v_or_b32_sdwa v11, v11, v5 dst_sel:DWORD dst_unused:UNUSED_PAD src0_sel:DWORD src1_sel:WORD_1
	v_or_b32_sdwa v10, v10, v12 dst_sel:DWORD dst_unused:UNUSED_PAD src0_sel:DWORD src1_sel:WORD_1
	ds_write_b64 v132, v[10:11] offset:4512
	v_mov_b32_e32 v10, v120
	v_mov_b32_e32 v11, v121
	v_mov_b32_e32 v12, v122
	v_mov_b32_e32 v13, v123
	v_mov_b32_e32 v15, v6
	v_mov_b32_e32 v6, v9
	v_mov_b32_e32 v14, v8
	v_pk_mul_f32 v[6:7], v[6:7], v[4:5] op_sel_hi:[1,0]
	v_pk_mul_f32 v[14:15], v[14:15], v[4:5] op_sel_hi:[1,0]
	v_mov_b32_e32 v17, v12
	v_mov_b32_e32 v12, v11
	v_mov_b32_e32 v16, v10
	v_pk_mul_f32 v[6:7], v[12:13], v[6:7]
	v_pk_mul_f32 v[14:15], v[16:17], v[14:15]
	v_and_b32_sdwa v9, v7, v213 dst_sel:DWORD dst_unused:UNUSED_PAD src0_sel:WORD_1 src1_sel:DWORD
	v_and_b32_sdwa v10, v6, v213 dst_sel:DWORD dst_unused:UNUSED_PAD src0_sel:WORD_1 src1_sel:DWORD
	v_and_b32_sdwa v5, v15, v213 dst_sel:DWORD dst_unused:UNUSED_PAD src0_sel:WORD_1 src1_sel:DWORD
	v_and_b32_sdwa v8, v14, v213 dst_sel:DWORD dst_unused:UNUSED_PAD src0_sel:WORD_1 src1_sel:DWORD
	v_add3_u32 v7, v7, v9, s76
	v_add3_u32 v6, v6, v10, s76
	v_add3_u32 v8, v14, v8, s76
	v_add3_u32 v5, v15, v5, s76
	v_and_b32_e32 v7, 0xffff0000, v7
	v_and_b32_e32 v6, 0xffff0000, v6
	v_or_b32_sdwa v7, v7, v5 dst_sel:DWORD dst_unused:UNUSED_PAD src0_sel:DWORD src1_sel:WORD_1
	v_or_b32_sdwa v6, v6, v8 dst_sel:DWORD dst_unused:UNUSED_PAD src0_sel:DWORD src1_sel:WORD_1
	ds_write_b64 v132, v[6:7] offset:4544
	v_mov_b32_e32 v6, v124
	v_mov_b32_e32 v7, v125
	v_mov_b32_e32 v8, v126
	v_mov_b32_e32 v9, v127
	v_mov_b32_e32 v11, v0
	v_mov_b32_e32 v0, v3
	v_mov_b32_e32 v10, v2
	v_pk_mul_f32 v[0:1], v[0:1], v[4:5] op_sel_hi:[1,0]
	v_pk_mul_f32 v[10:11], v[10:11], v[4:5] op_sel_hi:[1,0]
	v_mov_b32_e32 v13, v8
	v_mov_b32_e32 v8, v7
	v_mov_b32_e32 v12, v6
	v_pk_mul_f32 v[0:1], v[8:9], v[0:1]
	v_pk_mul_f32 v[10:11], v[12:13], v[10:11]
	v_and_b32_sdwa v4, v1, v213 dst_sel:DWORD dst_unused:UNUSED_PAD src0_sel:WORD_1 src1_sel:DWORD
	v_and_b32_sdwa v5, v0, v213 dst_sel:DWORD dst_unused:UNUSED_PAD src0_sel:WORD_1 src1_sel:DWORD
	v_and_b32_sdwa v2, v11, v213 dst_sel:DWORD dst_unused:UNUSED_PAD src0_sel:WORD_1 src1_sel:DWORD
	v_and_b32_sdwa v3, v10, v213 dst_sel:DWORD dst_unused:UNUSED_PAD src0_sel:WORD_1 src1_sel:DWORD
	v_add3_u32 v1, v1, v4, s76
	v_add3_u32 v0, v0, v5, s76
	v_add3_u32 v3, v10, v3, s76
	v_add3_u32 v2, v11, v2, s76
	v_and_b32_e32 v1, 0xffff0000, v1
	v_and_b32_e32 v0, 0xffff0000, v0
	v_or_b32_sdwa v1, v1, v2 dst_sel:DWORD dst_unused:UNUSED_PAD src0_sel:DWORD src1_sel:WORD_1
	v_or_b32_sdwa v0, v0, v3 dst_sel:DWORD dst_unused:UNUSED_PAD src0_sel:DWORD src1_sel:WORD_1
	ds_write_b64 v132, v[0:1] offset:4576
	s_waitcnt lgkmcnt(0)
	ds_read_b128 v[96:99], v133
	ds_read_b128 v[100:103], v133 offset:1088
	ds_read_b128 v[104:107], v133 offset:2176
	ds_read_b128 v[108:111], v133 offset:3264
	ds_read_b128 v[112:115], v133 offset:4352
	ds_read_b128 v[116:119], v133 offset:5440
	ds_read_b128 v[120:123], v133 offset:6528
	ds_read_b128 v[124:127], v133 offset:7616
	v_mov_b32_e32 v136, 0x4000
	v_mov_b32_e32 v137, 0
	s_waitcnt lgkmcnt(7)
	global_store_dwordx4 v[130:131], v[96:99], off
	v_lshl_add_u64 v[130:131], v[130:131], 0, v[136:137]
	s_waitcnt lgkmcnt(6)
	global_store_dwordx4 v[130:131], v[100:103], off
	v_lshl_add_u64 v[130:131], v[130:131], 0, v[136:137]
	s_waitcnt lgkmcnt(5)
	global_store_dwordx4 v[130:131], v[104:107], off
	v_lshl_add_u64 v[130:131], v[130:131], 0, v[136:137]
	s_waitcnt lgkmcnt(4)
	global_store_dwordx4 v[130:131], v[108:111], off
	v_lshl_add_u64 v[130:131], v[130:131], 0, v[136:137]
	s_waitcnt lgkmcnt(3)
	global_store_dwordx4 v[130:131], v[112:115], off
	v_lshl_add_u64 v[130:131], v[130:131], 0, v[136:137]
	s_waitcnt lgkmcnt(2)
	global_store_dwordx4 v[130:131], v[116:119], off
	v_lshl_add_u64 v[130:131], v[130:131], 0, v[136:137]
	s_waitcnt lgkmcnt(1)
	global_store_dwordx4 v[130:131], v[120:123], off
	v_lshl_add_u64 v[130:131], v[130:131], 0, v[136:137]
	s_waitcnt lgkmcnt(0)
	global_store_dwordx4 v[130:131], v[124:127], off
	s_cbranch_vccnz .LBB0_577

; __device__ __forceinline__ float rq_sum(float v) { v += __shfl_xor(v, 16); v += __shfl_xor(v, 32); return v; }
; __device__ __forceinline__ float frsq(float x) { return __builtin_amdgcn_rsqf(x); }
; __device__ __forceinline__ void attn_wg_task(const Frame& F, int l, int task) {
;     ...
;     for (int qb = 0; qb < 2; ++qb) {
;         const int tq = tq0 + qb * 16;
;         const float inv = 1.0f / rq_sum(l_run[qb]);
;         float ss = 0.f;
; #pragma unroll
;         for (int db = 0; db < 8; ++db) { O[qb][db] *= inv; ss += (O[qb][db][0] * O[qb][db][0] + O[qb][db][1] * O[qb][db][1]) + (O[qb][db][2] * O[qb][db][2] + O[qb][db][3] * O[qb][db][3]); }
;         const float rstd = frsq(rq_sum(ss) * (1.f / HD) + EPS);
; #pragma unroll
;         for (int db = 0; db < 8; ++db) {
;             const int d0 = h * HD + db * 16 + rq * 4;
;             const f32x4 g4 = ld_f4(F.attn_g + l * 1024 + d0);
.LBB0_549:
	ds_bpermute_b32 v64, v202, v151
	v_lshl_or_b32 v82, v204, 2, s19
	v_readlane_b32 s2, v251, 53
	v_readlane_b32 s3, v251, 54
	s_waitcnt lgkmcnt(0)
	v_add_f32_e32 v64, v151, v64
	ds_bpermute_b32 v65, v203, v64
	s_barrier
	s_waitcnt lgkmcnt(0)
	v_lshlrev_b32_e32 v184, 1, v82
	s_add_i32 s18, s18, s87
	v_add_f32_e32 v64, v64, v65
	v_div_scale_f32 v65, s[0:1], v64, v64, 1.0
	v_rcp_f32_e32 v66, v65
	s_nop 0
	v_fma_f32 v67, -v65, v66, 1.0
	v_fmac_f32_e32 v66, v67, v66
	v_div_scale_f32 v67, vcc, 1.0, v64, 1.0
	v_mul_f32_e32 v68, v67, v66
	v_fma_f32 v69, -v65, v68, v67
	v_fmac_f32_e32 v68, v69, v66
	v_fma_f32 v65, -v65, v68, v67
	v_div_fmas_f32 v65, v65, v66, v68
	v_div_fixup_f32 v84, v65, v64, 1.0
	v_pk_mul_f32 v[80:81], v[32:33], v[84:85] op_sel_hi:[1,0]
	v_pk_mul_f32 v[76:77], v[36:37], v[84:85] op_sel_hi:[1,0]
	v_pk_mul_f32 v[78:79], v[34:35], v[84:85] op_sel_hi:[1,0]
	v_pk_mul_f32 v[74:75], v[38:39], v[84:85] op_sel_hi:[1,0]
	v_mov_b32_e32 v34, v81
	v_mov_b32_e32 v35, v77
	v_mov_b32_e32 v32, v80
	v_mov_b32_e32 v33, v76
	v_pk_mul_f32 v[34:35], v[34:35], v[34:35]
	v_mov_b32_e32 v36, v79
	v_mov_b32_e32 v37, v75
	v_pk_fma_f32 v[32:33], v[32:33], v[32:33], v[34:35]
	v_mov_b32_e32 v34, v78
	v_mov_b32_e32 v35, v74
	v_pk_mul_f32 v[36:37], v[36:37], v[36:37]
	v_pk_mul_f32 v[72:73], v[40:41], v[84:85] op_sel_hi:[1,0]
	v_pk_fma_f32 v[34:35], v[34:35], v[34:35], v[36:37]
	v_pk_mul_f32 v[70:71], v[42:43], v[84:85] op_sel_hi:[1,0]
	v_pk_add_f32 v[32:33], v[32:33], v[34:35]
	v_pk_mul_f32 v[34:35], v[70:71], v[70:71]
	v_pk_add_f32 v[32:33], v[32:33], v[32:33] op_sel_hi:[0,1]
	v_pk_mul_f32 v[36:37], v[72:73], v[72:73]
	v_pk_mul_f32 v[68:69], v[44:45], v[84:85] op_sel_hi:[1,0]
	v_pk_mov_b32 v[38:39], v[36:37], v[34:35] op_sel:[1,0]
	v_mov_b32_e32 v37, v35
	v_pk_mul_f32 v[66:67], v[46:47], v[84:85] op_sel_hi:[1,0]
	v_mul_f32_e32 v32, v68, v68
	v_pk_add_f32 v[34:35], v[38:39], v[36:37]
	v_pk_fma_f32 v[36:37], v[68:69], v[68:69], v[32:33] op_sel_hi:[1,1,0]
	v_mul_f32_e32 v32, v66, v66
	v_pk_add_f32 v[34:35], v[34:35], v[34:35] op_sel_hi:[0,1]
	v_pk_fma_f32 v[38:39], v[66:67], v[66:67], v[32:33] op_sel_hi:[1,1,0]
	v_pk_mul_f32 v[50:51], v[50:51], v[84:85] op_sel_hi:[1,0]
	v_pk_mul_f32 v[64:65], v[48:49], v[84:85] op_sel_hi:[1,0]
	v_mul_f32_e32 v34, v50, v50
	v_mul_f32_e32 v36, v64, v64
	v_mul_f32_e32 v38, v65, v65
	v_mul_f32_e32 v32, v51, v51
	v_pk_add_f32 v[36:37], v[36:37], v[38:39]
	v_pk_add_f32 v[32:33], v[34:35], v[32:33]
	v_pk_mul_f32 v[48:49], v[52:53], v[84:85] op_sel_hi:[1,0]
	v_pk_add_f32 v[32:33], v[36:37], v[32:33]
	v_pk_mul_f32 v[46:47], v[54:55], v[84:85] op_sel_hi:[1,0]
	v_pk_add_f32 v[32:33], v[32:33], v[32:33] op_sel_hi:[0,1]
	v_pk_mul_f32 v[34:35], v[46:47], v[46:47]
	v_pk_mul_f32 v[36:37], v[48:49], v[48:49]
	v_pk_mul_f32 v[44:45], v[56:57], v[84:85] op_sel_hi:[1,0]
	v_pk_mov_b32 v[38:39], v[36:37], v[34:35] op_sel:[1,0]
	v_mov_b32_e32 v37, v35
	v_pk_mul_f32 v[42:43], v[58:59], v[84:85] op_sel_hi:[1,0]
	v_mul_f32_e32 v32, v44, v44
	v_pk_add_f32 v[34:35], v[38:39], v[36:37]
	v_pk_fma_f32 v[40:41], v[44:45], v[44:45], v[32:33] op_sel_hi:[1,1,0]
	v_mul_f32_e32 v32, v42, v42
	v_pk_add_f32 v[34:35], v[34:35], v[34:35] op_sel_hi:[0,1]
	v_pk_fma_f32 v[52:53], v[42:43], v[42:43], v[32:33] op_sel_hi:[1,1,0]
	v_pk_mul_f32 v[36:37], v[62:63], v[84:85] op_sel_hi:[1,0]
	v_pk_mul_f32 v[38:39], v[60:61], v[84:85] op_sel_hi:[1,0]
	v_mul_f32_e32 v34, v36, v36
	v_mul_f32_e32 v40, v38, v38
	v_mul_f32_e32 v52, v39, v39
	v_mul_f32_e32 v32, v37, v37
	v_pk_add_f32 v[40:41], v[40:41], v[52:53]
	v_pk_add_f32 v[32:33], v[34:35], v[32:33]
	v_lshlrev_b32_e32 v54, 2, v82
	global_load_dwordx4 v[96:99], v54, s[42:43]
	global_load_dwordx4 v[100:103], v54, s[42:43] offset:64
	global_load_dwordx4 v[104:107], v54, s[42:43] offset:128
	global_load_dwordx4 v[108:111], v54, s[42:43] offset:192
	global_load_dwordx4 v[112:115], v54, s[42:43] offset:256
	global_load_dwordx4 v[116:119], v54, s[42:43] offset:320
	global_load_dwordx4 v[120:123], v54, s[42:43] offset:384
	global_load_dwordx4 v[124:127], v54, s[42:43] offset:448
	v_pk_add_f32 v[32:33], v[40:41], v[32:33]
	v_mov_b32_e32 v56, v80
	v_add_f32_e32 v32, v32, v33
	ds_bpermute_b32 v33, v202, v32
	v_mov_b32_e32 v57, v78
	v_mov_b32_e32 v78, v81
	s_waitcnt lgkmcnt(0)
	v_add_f32_e32 v32, v32, v33
	ds_bpermute_b32 v33, v203, v32
	s_waitcnt lgkmcnt(0)
	v_add_f32_e32 v32, v32, v33
	v_fmamk_f32 v32, v32, 0x3c000000, v214
	v_rsq_f32_e32 v40, v32
	v_lshlrev_b64 v[32:33], 12, v[152:153]
	v_lshl_add_u64 v[52:53], s[2:3], 0, v[32:33]
	s_waitcnt vmcnt(0)
; __device__ __forceinline__ unsigned pk2(float lo, float hi) { return f2bf(lo) | (f2bf(hi) << 16); }
; __device__ __forceinline__ void attn_wg_task(const Frame& F, int l, int task) {
;     ...
; #pragma unroll
;         for (int db = 0; db < 8; ++db) {
;             const int d0 = h * HD + db * 16 + rq * 4;
;             const f32x4 g4 = ld_f4(F.attn_g + l * 1024 + d0);
;             u32x2 o; o.x = pk2(O[qb][db][0] * rstd * g4[0], O[qb][db][1] * rstd * g4[1]); o.y = pk2(O[qb][db][2] * rstd * g4[2], O[qb][db][3] * rstd * g4[3]);
;             st_u2(MIX + (size_t)tq * D + d0, o);
	v_mov_b32_e32 v32, v96
	v_mov_b32_e32 v33, v97
	v_mov_b32_e32 v34, v98
	v_mov_b32_e32 v35, v99
	v_pk_mul_f32 v[56:57], v[56:57], v[40:41] op_sel_hi:[1,0]
	v_mov_b32_e32 v58, v32
	v_mov_b32_e32 v59, v34
	v_pk_mul_f32 v[56:57], v[58:59], v[56:57]
	v_pk_mul_f32 v[58:59], v[78:79], v[40:41] op_sel_hi:[1,0]
	v_mov_b32_e32 v34, v33
	v_pk_mul_f32 v[32:33], v[34:35], v[58:59]
	v_and_b32_sdwa v35, v56, v213 dst_sel:DWORD dst_unused:UNUSED_PAD src0_sel:WORD_1 src1_sel:DWORD
	v_add3_u32 v41, v56, v35, s76
	v_and_b32_sdwa v35, v33, v213 dst_sel:DWORD dst_unused:UNUSED_PAD src0_sel:WORD_1 src1_sel:DWORD
	v_and_b32_sdwa v55, v32, v213 dst_sel:DWORD dst_unused:UNUSED_PAD src0_sel:WORD_1 src1_sel:DWORD
	v_and_b32_sdwa v34, v57, v213 dst_sel:DWORD dst_unused:UNUSED_PAD src0_sel:WORD_1 src1_sel:DWORD
	v_add3_u32 v33, v33, v35, s76
	v_add3_u32 v32, v32, v55, s76
	v_add3_u32 v34, v57, v34, s76
	v_and_b32_e32 v33, 0xffff0000, v33
	v_and_b32_e32 v32, 0xffff0000, v32
	v_or_b32_sdwa v35, v33, v34 dst_sel:DWORD dst_unused:UNUSED_PAD src0_sel:DWORD src1_sel:WORD_1
	v_or_b32_sdwa v34, v32, v41 dst_sel:DWORD dst_unused:UNUSED_PAD src0_sel:DWORD src1_sel:WORD_1
	v_lshl_add_u64 v[32:33], v[52:53], 0, v[184:185]
	v_and_b32_e32 v128, 15, v211
	v_lshrrev_b32_e32 v129, 4, v211
	v_lshrrev_b32_e32 v134, 6, v212
	v_mul_u32_u24_e32 v134, 0x2200, v134
	v_add_u32_e32 v134, v229, v134
	v_lshlrev_b32_e32 v135, 3, v129
	v_sub_u32_e32 v132, v134, v135
	v_lshlrev_b32_e32 v135, 8, v129
	v_add_u32_e32 v133, v134, v135
	v_lshlrev_b32_e32 v135, 8, v128
	v_sub_u32_e32 v133, v133, v135
	v_mul_u32_u24_e32 v135, 0xff8, v129
	v_mul_u32_u24_e32 v136, 0xff0, v128
	v_sub_u32_e32 v136, v135, v136
	v_ashrrev_i32_e32 v137, 31, v136
	v_lshl_add_u64 v[130:131], v[32:33], 0, v[136:137]
	ds_write_b64 v132, v[34:35]
	v_mov_b32_e32 v56, v100
	v_mov_b32_e32 v57, v101
	v_mov_b32_e32 v58, v102
	v_mov_b32_e32 v59, v103
	v_mov_b32_e32 v34, v76
	v_mov_b32_e32 v35, v74
	v_pk_mul_f32 v[34:35], v[34:35], v[40:41] op_sel_hi:[1,0]
	v_mov_b32_e32 v74, v77
	v_mov_b32_e32 v52, v56
	v_mov_b32_e32 v53, v58
	v_pk_mul_f32 v[34:35], v[52:53], v[34:35]
	v_pk_mul_f32 v[52:53], v[74:75], v[40:41] op_sel_hi:[1,0]
	v_mov_b32_e32 v58, v57
	v_pk_mul_f32 v[52:53], v[58:59], v[52:53]
	v_and_b32_sdwa v41, v35, v213 dst_sel:DWORD dst_unused:UNUSED_PAD src0_sel:WORD_1 src1_sel:DWORD
	v_and_b32_sdwa v55, v34, v213 dst_sel:DWORD dst_unused:UNUSED_PAD src0_sel:WORD_1 src1_sel:DWORD
	v_add3_u32 v34, v34, v55, s76
	v_add3_u32 v35, v35, v41, s76
	v_and_b32_sdwa v41, v53, v213 dst_sel:DWORD dst_unused:UNUSED_PAD src0_sel:WORD_1 src1_sel:DWORD
	v_and_b32_sdwa v55, v52, v213 dst_sel:DWORD dst_unused:UNUSED_PAD src0_sel:WORD_1 src1_sel:DWORD
	v_add3_u32 v41, v53, v41, s76
	v_add3_u32 v52, v52, v55, s76
	v_and_b32_e32 v41, 0xffff0000, v41
	v_and_b32_e32 v52, 0xffff0000, v52
	v_or_b32_sdwa v35, v41, v35 dst_sel:DWORD dst_unused:UNUSED_PAD src0_sel:DWORD src1_sel:WORD_1
	v_or_b32_sdwa v34, v52, v34 dst_sel:DWORD dst_unused:UNUSED_PAD src0_sel:DWORD src1_sel:WORD_1
	ds_write_b64 v132, v[34:35] offset:32
	v_mov_b32_e32 v56, v104
	v_mov_b32_e32 v57, v105
	v_mov_b32_e32 v58, v106
	v_mov_b32_e32 v59, v107
	v_mov_b32_e32 v34, v72
	v_mov_b32_e32 v35, v70
	v_pk_mul_f32 v[34:35], v[34:35], v[40:41] op_sel_hi:[1,0]
	v_mov_b32_e32 v70, v73
	v_mov_b32_e32 v52, v56
	v_mov_b32_e32 v53, v58
	v_pk_mul_f32 v[34:35], v[52:53], v[34:35]
	v_pk_mul_f32 v[52:53], v[70:71], v[40:41] op_sel_hi:[1,0]
	v_mov_b32_e32 v58, v57
	v_pk_mul_f32 v[52:53], v[58:59], v[52:53]
	v_and_b32_sdwa v41, v35, v213 dst_sel:DWORD dst_unused:UNUSED_PAD src0_sel:WORD_1 src1_sel:DWORD
	v_and_b32_sdwa v55, v34, v213 dst_sel:DWORD dst_unused:UNUSED_PAD src0_sel:WORD_1 src1_sel:DWORD
	v_add3_u32 v34, v34, v55, s76
	v_add3_u32 v35, v35, v41, s76
	v_and_b32_sdwa v41, v53, v213 dst_sel:DWORD dst_unused:UNUSED_PAD src0_sel:WORD_1 src1_sel:DWORD
	v_and_b32_sdwa v55, v52, v213 dst_sel:DWORD dst_unused:UNUSED_PAD src0_sel:WORD_1 src1_sel:DWORD
	v_add3_u32 v41, v53, v41, s76
	v_add3_u32 v52, v52, v55, s76
	v_and_b32_e32 v41, 0xffff0000, v41
	v_and_b32_e32 v52, 0xffff0000, v52
	v_or_b32_sdwa v35, v41, v35 dst_sel:DWORD dst_unused:UNUSED_PAD src0_sel:DWORD src1_sel:WORD_1
	v_or_b32_sdwa v34, v52, v34 dst_sel:DWORD dst_unused:UNUSED_PAD src0_sel:DWORD src1_sel:WORD_1
	ds_write_b64 v132, v[34:35] offset:64
	v_mov_b32_e32 v56, v108
	v_mov_b32_e32 v57, v109
	v_mov_b32_e32 v58, v110
	v_mov_b32_e32 v59, v111
	v_mov_b32_e32 v34, v68
	v_mov_b32_e32 v35, v66
	v_pk_mul_f32 v[34:35], v[34:35], v[40:41] op_sel_hi:[1,0]
	v_mov_b32_e32 v66, v69
	v_mov_b32_e32 v52, v56
	v_mov_b32_e32 v53, v58
	v_pk_mul_f32 v[34:35], v[52:53], v[34:35]
	v_pk_mul_f32 v[52:53], v[66:67], v[40:41] op_sel_hi:[1,0]
	v_mov_b32_e32 v58, v57
	v_pk_mul_f32 v[52:53], v[58:59], v[52:53]
	v_and_b32_sdwa v41, v35, v213 dst_sel:DWORD dst_unused:UNUSED_PAD src0_sel:WORD_1 src1_sel:DWORD
	v_and_b32_sdwa v55, v34, v213 dst_sel:DWORD dst_unused:UNUSED_PAD src0_sel:WORD_1 src1_sel:DWORD
	v_add3_u32 v34, v34, v55, s76
	v_add3_u32 v35, v35, v41, s76
	v_and_b32_sdwa v41, v53, v213 dst_sel:DWORD dst_unused:UNUSED_PAD src0_sel:WORD_1 src1_sel:DWORD
	v_and_b32_sdwa v55, v52, v213 dst_sel:DWORD dst_unused:UNUSED_PAD src0_sel:WORD_1 src1_sel:DWORD
	v_add3_u32 v41, v53, v41, s76
	v_add3_u32 v52, v52, v55, s76
	v_and_b32_e32 v41, 0xffff0000, v41
	v_and_b32_e32 v52, 0xffff0000, v52
	v_or_b32_sdwa v35, v41, v35 dst_sel:DWORD dst_unused:UNUSED_PAD src0_sel:DWORD src1_sel:WORD_1
	v_or_b32_sdwa v34, v52, v34 dst_sel:DWORD dst_unused:UNUSED_PAD src0_sel:DWORD src1_sel:WORD_1
	ds_write_b64 v132, v[34:35] offset:96
	v_mov_b32_e32 v56, v112
	v_mov_b32_e32 v57, v113
; __device__ __forceinline__ unsigned pk2(float lo, float hi) { return f2bf(lo) | (f2bf(hi) << 16); }
; __device__ __forceinline__ void attn_wg_task(const Frame& F, int l, int task) {
;     ...
; #pragma unroll
;         for (int db = 0; db < 8; ++db) {
;             const int d0 = h * HD + db * 16 + rq * 4;
;             const f32x4 g4 = ld_f4(F.attn_g + l * 1024 + d0);
;             u32x2 o; o.x = pk2(O[qb][db][0] * rstd * g4[0], O[qb][db][1] * rstd * g4[1]); o.y = pk2(O[qb][db][2] * rstd * g4[2], O[qb][db][3] * rstd * g4[3]);
;             st_u2(MIX + (size_t)tq * D + d0, o);
	v_mov_b32_e32 v58, v114
	v_mov_b32_e32 v59, v115
	v_mov_b32_e32 v34, v64
	v_mov_b32_e32 v35, v50
	v_pk_mul_f32 v[34:35], v[34:35], v[40:41] op_sel_hi:[1,0]
	v_mov_b32_e32 v50, v65
	v_pk_mul_f32 v[50:51], v[50:51], v[40:41] op_sel_hi:[1,0]
	v_mov_b32_e32 v52, v56
	v_mov_b32_e32 v53, v58
	v_pk_mul_f32 v[34:35], v[52:53], v[34:35]
	v_mov_b32_e32 v58, v57
	v_pk_mul_f32 v[50:51], v[58:59], v[50:51]
	v_and_b32_sdwa v41, v35, v213 dst_sel:DWORD dst_unused:UNUSED_PAD src0_sel:WORD_1 src1_sel:DWORD
	v_and_b32_sdwa v52, v34, v213 dst_sel:DWORD dst_unused:UNUSED_PAD src0_sel:WORD_1 src1_sel:DWORD
	v_add3_u32 v34, v34, v52, s76
	v_add3_u32 v35, v35, v41, s76
	v_and_b32_sdwa v41, v51, v213 dst_sel:DWORD dst_unused:UNUSED_PAD src0_sel:WORD_1 src1_sel:DWORD
	v_and_b32_sdwa v52, v50, v213 dst_sel:DWORD dst_unused:UNUSED_PAD src0_sel:WORD_1 src1_sel:DWORD
	v_add3_u32 v41, v51, v41, s76
	v_add3_u32 v50, v50, v52, s76
	v_and_b32_e32 v41, 0xffff0000, v41
	v_and_b32_e32 v50, 0xffff0000, v50
	v_or_b32_sdwa v35, v41, v35 dst_sel:DWORD dst_unused:UNUSED_PAD src0_sel:DWORD src1_sel:WORD_1
	v_or_b32_sdwa v34, v50, v34 dst_sel:DWORD dst_unused:UNUSED_PAD src0_sel:DWORD src1_sel:WORD_1
	ds_write_b64 v132, v[34:35] offset:128
	v_mov_b32_e32 v50, v116
	v_mov_b32_e32 v51, v117
	v_mov_b32_e32 v52, v118
	v_mov_b32_e32 v53, v119
	v_mov_b32_e32 v34, v48
	v_mov_b32_e32 v35, v46
	v_pk_mul_f32 v[34:35], v[34:35], v[40:41] op_sel_hi:[1,0]
	v_mov_b32_e32 v46, v49
	v_pk_mul_f32 v[46:47], v[46:47], v[40:41] op_sel_hi:[1,0]
	v_mov_b32_e32 v56, v50
	v_mov_b32_e32 v57, v52
	v_pk_mul_f32 v[34:35], v[56:57], v[34:35]
	v_mov_b32_e32 v52, v51
	v_pk_mul_f32 v[46:47], v[52:53], v[46:47]
	v_and_b32_sdwa v41, v35, v213 dst_sel:DWORD dst_unused:UNUSED_PAD src0_sel:WORD_1 src1_sel:DWORD
	v_and_b32_sdwa v48, v34, v213 dst_sel:DWORD dst_unused:UNUSED_PAD src0_sel:WORD_1 src1_sel:DWORD
	v_add3_u32 v34, v34, v48, s76
	v_add3_u32 v35, v35, v41, s76
	v_and_b32_sdwa v41, v47, v213 dst_sel:DWORD dst_unused:UNUSED_PAD src0_sel:WORD_1 src1_sel:DWORD
	v_and_b32_sdwa v48, v46, v213 dst_sel:DWORD dst_unused:UNUSED_PAD src0_sel:WORD_1 src1_sel:DWORD
	v_add3_u32 v41, v47, v41, s76
	v_add3_u32 v46, v46, v48, s76
	v_and_b32_e32 v41, 0xffff0000, v41
	v_and_b32_e32 v46, 0xffff0000, v46
	v_or_b32_sdwa v35, v41, v35 dst_sel:DWORD dst_unused:UNUSED_PAD src0_sel:DWORD src1_sel:WORD_1
	v_or_b32_sdwa v34, v46, v34 dst_sel:DWORD dst_unused:UNUSED_PAD src0_sel:DWORD src1_sel:WORD_1
	ds_write_b64 v132, v[34:35] offset:160
	v_mov_b32_e32 v46, v120
	v_mov_b32_e32 v47, v121
	v_mov_b32_e32 v48, v122
	v_mov_b32_e32 v49, v123
	v_mov_b32_e32 v34, v44
	v_mov_b32_e32 v35, v42
	v_pk_mul_f32 v[34:35], v[34:35], v[40:41] op_sel_hi:[1,0]
	v_mov_b32_e32 v42, v45
	v_pk_mul_f32 v[42:43], v[42:43], v[40:41] op_sel_hi:[1,0]
	v_mov_b32_e32 v50, v46
	v_mov_b32_e32 v51, v48
	v_pk_mul_f32 v[34:35], v[50:51], v[34:35]
	v_mov_b32_e32 v48, v47
	v_pk_mul_f32 v[42:43], v[48:49], v[42:43]
	v_and_b32_sdwa v41, v35, v213 dst_sel:DWORD dst_unused:UNUSED_PAD src0_sel:WORD_1 src1_sel:DWORD
	v_and_b32_sdwa v44, v34, v213 dst_sel:DWORD dst_unused:UNUSED_PAD src0_sel:WORD_1 src1_sel:DWORD
	v_add3_u32 v34, v34, v44, s76
	v_add3_u32 v35, v35, v41, s76
	v_and_b32_sdwa v41, v43, v213 dst_sel:DWORD dst_unused:UNUSED_PAD src0_sel:WORD_1 src1_sel:DWORD
	v_and_b32_sdwa v44, v42, v213 dst_sel:DWORD dst_unused:UNUSED_PAD src0_sel:WORD_1 src1_sel:DWORD
	v_add3_u32 v41, v43, v41, s76
	v_add3_u32 v42, v42, v44, s76
	v_and_b32_e32 v41, 0xffff0000, v41
	v_and_b32_e32 v42, 0xffff0000, v42
	v_or_b32_sdwa v35, v41, v35 dst_sel:DWORD dst_unused:UNUSED_PAD src0_sel:DWORD src1_sel:WORD_1
	v_or_b32_sdwa v34, v42, v34 dst_sel:DWORD dst_unused:UNUSED_PAD src0_sel:DWORD src1_sel:WORD_1
	ds_write_b64 v132, v[34:35] offset:192
	v_mov_b32_e32 v42, v124
	v_mov_b32_e32 v43, v125
	v_mov_b32_e32 v44, v126
	v_mov_b32_e32 v45, v127
	v_mov_b32_e32 v34, v38
	v_mov_b32_e32 v35, v36
	v_pk_mul_f32 v[34:35], v[34:35], v[40:41] op_sel_hi:[1,0]
	v_mov_b32_e32 v36, v39
	v_pk_mul_f32 v[36:37], v[36:37], v[40:41] op_sel_hi:[1,0]
	v_mov_b32_e32 v46, v42
	v_mov_b32_e32 v47, v44
	v_pk_mul_f32 v[34:35], v[46:47], v[34:35]
	v_mov_b32_e32 v44, v43
	v_pk_mul_f32 v[36:37], v[44:45], v[36:37]
	v_and_b32_sdwa v38, v35, v213 dst_sel:DWORD dst_unused:UNUSED_PAD src0_sel:WORD_1 src1_sel:DWORD
	v_and_b32_sdwa v39, v34, v213 dst_sel:DWORD dst_unused:UNUSED_PAD src0_sel:WORD_1 src1_sel:DWORD
	v_add3_u32 v34, v34, v39, s76
	v_add3_u32 v35, v35, v38, s76
	v_and_b32_sdwa v38, v37, v213 dst_sel:DWORD dst_unused:UNUSED_PAD src0_sel:WORD_1 src1_sel:DWORD
	v_and_b32_sdwa v39, v36, v213 dst_sel:DWORD dst_unused:UNUSED_PAD src0_sel:WORD_1 src1_sel:DWORD
	v_add3_u32 v37, v37, v38, s76
	v_add3_u32 v36, v36, v39, s76
	v_and_b32_e32 v37, 0xffff0000, v37
	v_and_b32_e32 v36, 0xffff0000, v36
	v_or_b32_sdwa v35, v37, v35 dst_sel:DWORD dst_unused:UNUSED_PAD src0_sel:DWORD src1_sel:WORD_1
	v_or_b32_sdwa v34, v36, v34 dst_sel:DWORD dst_unused:UNUSED_PAD src0_sel:DWORD src1_sel:WORD_1
	ds_write_b64 v132, v[34:35] offset:224
	ds_bpermute_b32 v32, v202, v150
	s_waitcnt lgkmcnt(0)
	v_add_f32_e32 v32, v150, v32
	ds_bpermute_b32 v33, v203, v32
	s_waitcnt lgkmcnt(0)
; __device__ __forceinline__ unsigned pk2(float lo, float hi) { return f2bf(lo) | (f2bf(hi) << 16); }
; __device__ __forceinline__ float rq_sum(float v) { v += __shfl_xor(v, 16); v += __shfl_xor(v, 32); return v; }
; __device__ __forceinline__ float frsq(float x) { return __builtin_amdgcn_rsqf(x); }
; __device__ __forceinline__ void attn_wg_task(const Frame& F, int l, int task) {
;     ...
;     for (int qb = 0; qb < 2; ++qb) {
;         const int tq = tq0 + qb * 16;
;         const float inv = 1.0f / rq_sum(l_run[qb]);
;         float ss = 0.f;
; #pragma unroll
;         for (int db = 0; db < 8; ++db) { O[qb][db] *= inv; ss += (O[qb][db][0] * O[qb][db][0] + O[qb][db][1] * O[qb][db][1]) + (O[qb][db][2] * O[qb][db][2] + O[qb][db][3] * O[qb][db][3]); }
;         const float rstd = frsq(rq_sum(ss) * (1.f / HD) + EPS);
; #pragma unroll
;         for (int db = 0; db < 8; ++db) {
;             const int d0 = h * HD + db * 16 + rq * 4;
;             const f32x4 g4 = ld_f4(F.attn_g + l * 1024 + d0);
;             u32x2 o; o.x = pk2(O[qb][db][0] * rstd * g4[0], O[qb][db][1] * rstd * g4[1]); o.y = pk2(O[qb][db][2] * rstd * g4[2], O[qb][db][3] * rstd * g4[3]);
;             st_u2(MIX + (size_t)tq * D + d0, o);
;         }
	v_add_f32_e32 v32, v32, v33
	v_div_scale_f32 v33, s[0:1], v32, v32, 1.0
	v_rcp_f32_e32 v34, v33
	v_readlane_b32 s0, v250, 0
	s_add_i32 s17, s17, s0
	v_readlane_b32 s0, v250, 2
	v_fma_f32 v35, -v33, v34, 1.0
	v_fmac_f32_e32 v34, v35, v34
	v_div_scale_f32 v35, vcc, 1.0, v32, 1.0
	v_mul_f32_e32 v36, v35, v34
	v_fma_f32 v37, -v33, v36, v35
	v_fmac_f32_e32 v36, v37, v34
	v_fma_f32 v33, -v33, v36, v35
	v_div_fmas_f32 v33, v33, v34, v36
	v_div_fixup_f32 v48, v33, v32, 1.0
	v_pk_mul_f32 v[46:47], v[4:5], v[48:49] op_sel_hi:[1,0]
	v_pk_mul_f32 v[42:43], v[8:9], v[48:49] op_sel_hi:[1,0]
	v_pk_mul_f32 v[44:45], v[6:7], v[48:49] op_sel_hi:[1,0]
	v_pk_mul_f32 v[36:37], v[10:11], v[48:49] op_sel_hi:[1,0]
	v_mov_b32_e32 v6, v47
	v_mov_b32_e32 v7, v43
	v_mov_b32_e32 v4, v46
	v_mov_b32_e32 v5, v42
	v_pk_mul_f32 v[6:7], v[6:7], v[6:7]
	v_mov_b32_e32 v8, v45
	v_mov_b32_e32 v9, v37
	v_pk_fma_f32 v[4:5], v[4:5], v[4:5], v[6:7]
	v_mov_b32_e32 v6, v44
	v_mov_b32_e32 v7, v36
	v_pk_mul_f32 v[8:9], v[8:9], v[8:9]
	v_pk_mul_f32 v[40:41], v[0:1], v[48:49] op_sel_hi:[1,0]
	v_pk_mul_f32 v[38:39], v[2:3], v[48:49] op_sel_hi:[1,0]
	v_pk_fma_f32 v[6:7], v[6:7], v[6:7], v[8:9]
	v_pk_mul_f32 v[0:1], v[38:39], v[38:39]
	v_pk_mul_f32 v[2:3], v[40:41], v[40:41]
	v_pk_add_f32 v[4:5], v[4:5], v[6:7]
	v_pk_mov_b32 v[6:7], v[2:3], v[0:1] op_sel:[1,0]
	v_mov_b32_e32 v3, v1
	v_pk_add_f32 v[0:1], v[6:7], v[2:3]
	v_pk_mul_f32 v[34:35], v[12:13], v[48:49] op_sel_hi:[1,0]
	v_pk_add_f32 v[0:1], v[0:1], v[0:1] op_sel_hi:[0,1]
	v_pk_mul_f32 v[32:33], v[14:15], v[48:49] op_sel_hi:[1,0]
	v_mul_f32_e32 v0, v34, v34
	v_pk_fma_f32 v[2:3], v[34:35], v[34:35], v[0:1] op_sel_hi:[1,1,0]
	v_mul_f32_e32 v0, v32, v32
	v_pk_add_f32 v[4:5], v[4:5], v[4:5] op_sel_hi:[0,1]
	v_pk_fma_f32 v[6:7], v[32:33], v[32:33], v[0:1] op_sel_hi:[1,1,0]
	v_pk_mul_f32 v[14:15], v[18:19], v[48:49] op_sel_hi:[1,0]
	v_pk_mul_f32 v[16:17], v[16:17], v[48:49] op_sel_hi:[1,0]
	v_mul_f32_e32 v0, v14, v14
	v_mul_f32_e32 v2, v16, v16
	v_mul_f32_e32 v6, v17, v17
	v_mul_f32_e32 v4, v15, v15
	v_pk_add_f32 v[2:3], v[2:3], v[6:7]
	v_pk_add_f32 v[0:1], v[0:1], v[4:5]
	v_pk_mul_f32 v[12:13], v[20:21], v[48:49] op_sel_hi:[1,0]
	v_pk_add_f32 v[0:1], v[2:3], v[0:1]
	v_pk_mul_f32 v[10:11], v[22:23], v[48:49] op_sel_hi:[1,0]
	v_pk_add_f32 v[4:5], v[0:1], v[0:1] op_sel_hi:[0,1]
	v_pk_mul_f32 v[0:1], v[10:11], v[10:11]
	v_pk_mul_f32 v[2:3], v[12:13], v[12:13]
	v_pk_mul_f32 v[8:9], v[24:25], v[48:49] op_sel_hi:[1,0]
	v_pk_mov_b32 v[6:7], v[2:3], v[0:1] op_sel:[1,0]
	v_mov_b32_e32 v3, v1
	v_pk_add_f32 v[0:1], v[6:7], v[2:3]
	v_pk_mul_f32 v[6:7], v[26:27], v[48:49] op_sel_hi:[1,0]
	v_pk_add_f32 v[18:19], v[0:1], v[0:1] op_sel_hi:[0,1]
	v_mul_f32_e32 v0, v8, v8
	v_pk_fma_f32 v[20:21], v[8:9], v[8:9], v[0:1] op_sel_hi:[1,1,0]
	v_mul_f32_e32 v0, v6, v6
	v_pk_fma_f32 v[22:23], v[6:7], v[6:7], v[0:1] op_sel_hi:[1,1,0]
	v_pk_mul_f32 v[0:1], v[30:31], v[48:49] op_sel_hi:[1,0]
	v_pk_mul_f32 v[2:3], v[28:29], v[48:49] op_sel_hi:[1,0]
	v_mul_f32_e32 v18, v0, v0
	v_mul_f32_e32 v20, v2, v2
	v_mul_f32_e32 v22, v3, v3
	v_mul_f32_e32 v4, v1, v1
	v_pk_add_f32 v[20:21], v[20:21], v[22:23]
	v_pk_add_f32 v[4:5], v[18:19], v[4:5]
	v_mov_b32_e32 v24, v46
	v_pk_add_f32 v[4:5], v[20:21], v[4:5]
	v_mov_b32_e32 v20, v96
	v_mov_b32_e32 v21, v97
	v_mov_b32_e32 v22, v98
	v_mov_b32_e32 v23, v99
	v_add_f32_e32 v4, v4, v5
	ds_bpermute_b32 v5, v202, v4
	v_mov_b32_e32 v25, v44
	v_mov_b32_e32 v44, v47
	v_lshlrev_b64 v[18:19], 12, v[148:149]
	v_lshl_add_u64 v[18:19], s[2:3], 0, v[18:19]
	s_waitcnt lgkmcnt(0)
	v_add_f32_e32 v4, v4, v5
	ds_bpermute_b32 v5, v203, v4
	v_lshl_add_u64 v[18:19], v[18:19], 0, v[184:185]
	s_add_i32 s16, s16, s0
	s_cmpk_lt_i32 s18, 0x200
	s_waitcnt lgkmcnt(0)
	v_add_f32_e32 v4, v4, v5
	v_fmamk_f32 v4, v4, 0x3c000000, v214
	v_rsq_f32_e32 v4, v4
	v_mov_b32_e32 v26, v20
	v_pk_mul_f32 v[24:25], v[24:25], v[4:5] op_sel_hi:[1,0]
	v_mov_b32_e32 v27, v22
	v_pk_mul_f32 v[24:25], v[26:27], v[24:25]
	v_pk_mul_f32 v[26:27], v[44:45], v[4:5] op_sel_hi:[1,0]
	v_mov_b32_e32 v22, v21
	v_pk_mul_f32 v[20:21], v[22:23], v[26:27]
	v_and_b32_sdwa v22, v24, v213 dst_sel:DWORD dst_unused:UNUSED_PAD src0_sel:WORD_1 src1_sel:DWORD
	v_add3_u32 v22, v24, v22, s76
	v_and_b32_sdwa v23, v21, v213 dst_sel:DWORD dst_unused:UNUSED_PAD src0_sel:WORD_1 src1_sel:DWORD
	v_and_b32_sdwa v24, v20, v213 dst_sel:DWORD dst_unused:UNUSED_PAD src0_sel:WORD_1 src1_sel:DWORD
	v_and_b32_sdwa v5, v25, v213 dst_sel:DWORD dst_unused:UNUSED_PAD src0_sel:WORD_1 src1_sel:DWORD
	v_add3_u32 v21, v21, v23, s76
	v_add3_u32 v20, v20, v24, s76
	v_add3_u32 v5, v25, v5, s76
	v_and_b32_e32 v21, 0xffff0000, v21
	v_and_b32_e32 v20, 0xffff0000, v20
	v_or_b32_sdwa v21, v21, v5 dst_sel:DWORD dst_unused:UNUSED_PAD src0_sel:DWORD src1_sel:WORD_1
	v_or_b32_sdwa v20, v20, v22 dst_sel:DWORD dst_unused:UNUSED_PAD src0_sel:DWORD src1_sel:WORD_1
	ds_write_b64 v132, v[20:21] offset:4352
	v_mov_b32_e32 v20, v100
	v_mov_b32_e32 v21, v101
	v_mov_b32_e32 v22, v102
	v_mov_b32_e32 v23, v103
	v_mov_b32_e32 v24, v42
	v_mov_b32_e32 v25, v36
	v_pk_mul_f32 v[24:25], v[24:25], v[4:5] op_sel_hi:[1,0]
	v_mov_b32_e32 v36, v43
	v_mov_b32_e32 v26, v20
	v_mov_b32_e32 v27, v22
	v_pk_mul_f32 v[24:25], v[26:27], v[24:25]
	v_pk_mul_f32 v[26:27], v[36:37], v[4:5] op_sel_hi:[1,0]
	v_mov_b32_e32 v22, v21
	v_pk_mul_f32 v[20:21], v[22:23], v[26:27]
	v_and_b32_sdwa v22, v24, v213 dst_sel:DWORD dst_unused:UNUSED_PAD src0_sel:WORD_1 src1_sel:DWORD
	v_add3_u32 v22, v24, v22, s76
	v_and_b32_sdwa v23, v21, v213 dst_sel:DWORD dst_unused:UNUSED_PAD src0_sel:WORD_1 src1_sel:DWORD
	v_and_b32_sdwa v24, v20, v213 dst_sel:DWORD dst_unused:UNUSED_PAD src0_sel:WORD_1 src1_sel:DWORD
; __device__ __forceinline__ unsigned pk2(float lo, float hi) { return f2bf(lo) | (f2bf(hi) << 16); }
; __device__ __forceinline__ void attn_wg_task(const Frame& F, int l, int task) {
;     ...
;         for (int db = 0; db < 8; ++db) {
;             const int d0 = h * HD + db * 16 + rq * 4;
;             const f32x4 g4 = ld_f4(F.attn_g + l * 1024 + d0);
;             u32x2 o; o.x = pk2(O[qb][db][0] * rstd * g4[0], O[qb][db][1] * rstd * g4[1]); o.y = pk2(O[qb][db][2] * rstd * g4[2], O[qb][db][3] * rstd * g4[3]);
;             st_u2(MIX + (size_t)tq * D + d0, o);
;         }
	v_and_b32_sdwa v5, v25, v213 dst_sel:DWORD dst_unused:UNUSED_PAD src0_sel:WORD_1 src1_sel:DWORD
	v_add3_u32 v21, v21, v23, s76
	v_add3_u32 v20, v20, v24, s76
	v_add3_u32 v5, v25, v5, s76
	v_and_b32_e32 v21, 0xffff0000, v21
	v_and_b32_e32 v20, 0xffff0000, v20
	v_or_b32_sdwa v21, v21, v5 dst_sel:DWORD dst_unused:UNUSED_PAD src0_sel:DWORD src1_sel:WORD_1
	v_or_b32_sdwa v20, v20, v22 dst_sel:DWORD dst_unused:UNUSED_PAD src0_sel:DWORD src1_sel:WORD_1
	ds_write_b64 v132, v[20:21] offset:4384
	v_mov_b32_e32 v20, v104
	v_mov_b32_e32 v21, v105
	v_mov_b32_e32 v22, v106
	v_mov_b32_e32 v23, v107
	v_mov_b32_e32 v24, v40
	v_mov_b32_e32 v25, v38
	v_pk_mul_f32 v[24:25], v[24:25], v[4:5] op_sel_hi:[1,0]
	v_mov_b32_e32 v38, v41
	v_mov_b32_e32 v26, v20
	v_mov_b32_e32 v27, v22
	v_pk_mul_f32 v[24:25], v[26:27], v[24:25]
	v_pk_mul_f32 v[26:27], v[38:39], v[4:5] op_sel_hi:[1,0]
	v_mov_b32_e32 v22, v21
	v_pk_mul_f32 v[20:21], v[22:23], v[26:27]
	v_and_b32_sdwa v22, v24, v213 dst_sel:DWORD dst_unused:UNUSED_PAD src0_sel:WORD_1 src1_sel:DWORD
	v_add3_u32 v22, v24, v22, s76
	v_and_b32_sdwa v23, v21, v213 dst_sel:DWORD dst_unused:UNUSED_PAD src0_sel:WORD_1 src1_sel:DWORD
	v_and_b32_sdwa v24, v20, v213 dst_sel:DWORD dst_unused:UNUSED_PAD src0_sel:WORD_1 src1_sel:DWORD
	v_and_b32_sdwa v5, v25, v213 dst_sel:DWORD dst_unused:UNUSED_PAD src0_sel:WORD_1 src1_sel:DWORD
	v_add3_u32 v21, v21, v23, s76
	v_add3_u32 v20, v20, v24, s76
	v_add3_u32 v5, v25, v5, s76
	v_and_b32_e32 v21, 0xffff0000, v21
	v_and_b32_e32 v20, 0xffff0000, v20
	v_or_b32_sdwa v21, v21, v5 dst_sel:DWORD dst_unused:UNUSED_PAD src0_sel:DWORD src1_sel:WORD_1
	v_or_b32_sdwa v20, v20, v22 dst_sel:DWORD dst_unused:UNUSED_PAD src0_sel:DWORD src1_sel:WORD_1
	ds_write_b64 v132, v[20:21] offset:4416
	v_mov_b32_e32 v20, v108
	v_mov_b32_e32 v21, v109
	v_mov_b32_e32 v22, v110
	v_mov_b32_e32 v23, v111
	v_mov_b32_e32 v24, v34
	v_mov_b32_e32 v25, v32
	v_pk_mul_f32 v[24:25], v[24:25], v[4:5] op_sel_hi:[1,0]
	v_mov_b32_e32 v32, v35
	v_mov_b32_e32 v26, v20
	v_mov_b32_e32 v27, v22
	v_pk_mul_f32 v[24:25], v[26:27], v[24:25]
	v_pk_mul_f32 v[26:27], v[32:33], v[4:5] op_sel_hi:[1,0]
	v_mov_b32_e32 v22, v21
	v_pk_mul_f32 v[20:21], v[22:23], v[26:27]
	v_and_b32_sdwa v22, v24, v213 dst_sel:DWORD dst_unused:UNUSED_PAD src0_sel:WORD_1 src1_sel:DWORD
	v_add3_u32 v22, v24, v22, s76
	v_and_b32_sdwa v23, v21, v213 dst_sel:DWORD dst_unused:UNUSED_PAD src0_sel:WORD_1 src1_sel:DWORD
	v_and_b32_sdwa v24, v20, v213 dst_sel:DWORD dst_unused:UNUSED_PAD src0_sel:WORD_1 src1_sel:DWORD
	v_and_b32_sdwa v5, v25, v213 dst_sel:DWORD dst_unused:UNUSED_PAD src0_sel:WORD_1 src1_sel:DWORD
	v_add3_u32 v21, v21, v23, s76
	v_add3_u32 v20, v20, v24, s76
	v_add3_u32 v5, v25, v5, s76
	v_and_b32_e32 v21, 0xffff0000, v21
	v_and_b32_e32 v20, 0xffff0000, v20
	v_or_b32_sdwa v21, v21, v5 dst_sel:DWORD dst_unused:UNUSED_PAD src0_sel:DWORD src1_sel:WORD_1
	v_or_b32_sdwa v20, v20, v22 dst_sel:DWORD dst_unused:UNUSED_PAD src0_sel:DWORD src1_sel:WORD_1
	ds_write_b64 v132, v[20:21] offset:4448
	v_mov_b32_e32 v20, v112
	v_mov_b32_e32 v21, v113
	v_mov_b32_e32 v22, v114
	v_mov_b32_e32 v23, v115
	v_mov_b32_e32 v25, v14
	v_mov_b32_e32 v14, v17
	v_mov_b32_e32 v24, v16
	v_pk_mul_f32 v[14:15], v[14:15], v[4:5] op_sel_hi:[1,0]
	v_pk_mul_f32 v[24:25], v[24:25], v[4:5] op_sel_hi:[1,0]
	v_mov_b32_e32 v27, v22
	v_mov_b32_e32 v22, v21
	v_mov_b32_e32 v26, v20
	v_pk_mul_f32 v[14:15], v[22:23], v[14:15]
	v_pk_mul_f32 v[24:25], v[26:27], v[24:25]
	v_and_b32_sdwa v17, v15, v213 dst_sel:DWORD dst_unused:UNUSED_PAD src0_sel:WORD_1 src1_sel:DWORD
	v_and_b32_sdwa v20, v14, v213 dst_sel:DWORD dst_unused:UNUSED_PAD src0_sel:WORD_1 src1_sel:DWORD
	v_and_b32_sdwa v5, v25, v213 dst_sel:DWORD dst_unused:UNUSED_PAD src0_sel:WORD_1 src1_sel:DWORD
	v_and_b32_sdwa v16, v24, v213 dst_sel:DWORD dst_unused:UNUSED_PAD src0_sel:WORD_1 src1_sel:DWORD
	v_add3_u32 v15, v15, v17, s76
	v_add3_u32 v14, v14, v20, s76
	v_add3_u32 v16, v24, v16, s76
	v_add3_u32 v5, v25, v5, s76
	v_and_b32_e32 v15, 0xffff0000, v15
	v_and_b32_e32 v14, 0xffff0000, v14
	v_or_b32_sdwa v15, v15, v5 dst_sel:DWORD dst_unused:UNUSED_PAD src0_sel:DWORD src1_sel:WORD_1
	v_or_b32_sdwa v14, v14, v16 dst_sel:DWORD dst_unused:UNUSED_PAD src0_sel:DWORD src1_sel:WORD_1
	ds_write_b64 v132, v[14:15] offset:4480
	v_mov_b32_e32 v14, v116
	v_mov_b32_e32 v15, v117
	v_mov_b32_e32 v16, v118
	v_mov_b32_e32 v17, v119
	v_mov_b32_e32 v21, v10
	v_mov_b32_e32 v10, v13
	v_mov_b32_e32 v20, v12
	v_pk_mul_f32 v[10:11], v[10:11], v[4:5] op_sel_hi:[1,0]
	v_pk_mul_f32 v[20:21], v[20:21], v[4:5] op_sel_hi:[1,0]
	v_mov_b32_e32 v23, v16
	v_mov_b32_e32 v16, v15
	v_mov_b32_e32 v22, v14
	v_pk_mul_f32 v[10:11], v[16:17], v[10:11]
; __device__ __forceinline__ unsigned pk2(float lo, float hi) { return f2bf(lo) | (f2bf(hi) << 16); }
; __device__ __forceinline__ void attn_wg_task(const Frame& F, int l, int task) {
;     ...
;         for (int db = 0; db < 8; ++db) {
;             const int d0 = h * HD + db * 16 + rq * 4;
;             const f32x4 g4 = ld_f4(F.attn_g + l * 1024 + d0);
;             u32x2 o; o.x = pk2(O[qb][db][0] * rstd * g4[0], O[qb][db][1] * rstd * g4[1]); o.y = pk2(O[qb][db][2] * rstd * g4[2], O[qb][db][3] * rstd * g4[3]);
;             st_u2(MIX + (size_t)tq * D + d0, o);
;         }
	v_pk_mul_f32 v[20:21], v[22:23], v[20:21]
	v_and_b32_sdwa v13, v11, v213 dst_sel:DWORD dst_unused:UNUSED_PAD src0_sel:WORD_1 src1_sel:DWORD
	v_and_b32_sdwa v14, v10, v213 dst_sel:DWORD dst_unused:UNUSED_PAD src0_sel:WORD_1 src1_sel:DWORD
	v_and_b32_sdwa v5, v21, v213 dst_sel:DWORD dst_unused:UNUSED_PAD src0_sel:WORD_1 src1_sel:DWORD
	v_and_b32_sdwa v12, v20, v213 dst_sel:DWORD dst_unused:UNUSED_PAD src0_sel:WORD_1 src1_sel:DWORD
	v_add3_u32 v11, v11, v13, s76
	v_add3_u32 v10, v10, v14, s76
	v_add3_u32 v12, v20, v12, s76
	v_add3_u32 v5, v21, v5, s76
	v_and_b32_e32 v11, 0xffff0000, v11
	v_and_b32_e32 v10, 0xffff0000, v10
	v_or_b32_sdwa v11, v11, v5 dst_sel:DWORD dst_unused:UNUSED_PAD src0_sel:DWORD src1_sel:WORD_1
	v_or_b32_sdwa v10, v10, v12 dst_sel:DWORD dst_unused:UNUSED_PAD src0_sel:DWORD src1_sel:WORD_1
	ds_write_b64 v132, v[10:11] offset:4512
	v_mov_b32_e32 v10, v120
	v_mov_b32_e32 v11, v121
	v_mov_b32_e32 v12, v122
	v_mov_b32_e32 v13, v123
	v_mov_b32_e32 v15, v6
	v_mov_b32_e32 v6, v9
	v_mov_b32_e32 v14, v8
	v_pk_mul_f32 v[6:7], v[6:7], v[4:5] op_sel_hi:[1,0]
	v_pk_mul_f32 v[14:15], v[14:15], v[4:5] op_sel_hi:[1,0]
	v_mov_b32_e32 v17, v12
	v_mov_b32_e32 v12, v11
	v_mov_b32_e32 v16, v10
	v_pk_mul_f32 v[6:7], v[12:13], v[6:7]
	v_pk_mul_f32 v[14:15], v[16:17], v[14:15]
	v_and_b32_sdwa v9, v7, v213 dst_sel:DWORD dst_unused:UNUSED_PAD src0_sel:WORD_1 src1_sel:DWORD
	v_and_b32_sdwa v10, v6, v213 dst_sel:DWORD dst_unused:UNUSED_PAD src0_sel:WORD_1 src1_sel:DWORD
	v_and_b32_sdwa v5, v15, v213 dst_sel:DWORD dst_unused:UNUSED_PAD src0_sel:WORD_1 src1_sel:DWORD
	v_and_b32_sdwa v8, v14, v213 dst_sel:DWORD dst_unused:UNUSED_PAD src0_sel:WORD_1 src1_sel:DWORD
	v_add3_u32 v7, v7, v9, s76
	v_add3_u32 v6, v6, v10, s76
	v_add3_u32 v8, v14, v8, s76
	v_add3_u32 v5, v15, v5, s76
	v_and_b32_e32 v7, 0xffff0000, v7
	v_and_b32_e32 v6, 0xffff0000, v6
	v_or_b32_sdwa v7, v7, v5 dst_sel:DWORD dst_unused:UNUSED_PAD src0_sel:DWORD src1_sel:WORD_1
	v_or_b32_sdwa v6, v6, v8 dst_sel:DWORD dst_unused:UNUSED_PAD src0_sel:DWORD src1_sel:WORD_1
	ds_write_b64 v132, v[6:7] offset:4544
	v_mov_b32_e32 v6, v124
	v_mov_b32_e32 v7, v125
	v_mov_b32_e32 v8, v126
	v_mov_b32_e32 v9, v127
	v_mov_b32_e32 v11, v0
	v_mov_b32_e32 v0, v3
	v_mov_b32_e32 v10, v2
	v_pk_mul_f32 v[0:1], v[0:1], v[4:5] op_sel_hi:[1,0]
	v_pk_mul_f32 v[10:11], v[10:11], v[4:5] op_sel_hi:[1,0]
	v_mov_b32_e32 v13, v8
	v_mov_b32_e32 v8, v7
	v_mov_b32_e32 v12, v6
	v_pk_mul_f32 v[0:1], v[8:9], v[0:1]
	v_pk_mul_f32 v[10:11], v[12:13], v[10:11]
	v_and_b32_sdwa v4, v1, v213 dst_sel:DWORD dst_unused:UNUSED_PAD src0_sel:WORD_1 src1_sel:DWORD
	v_and_b32_sdwa v5, v0, v213 dst_sel:DWORD dst_unused:UNUSED_PAD src0_sel:WORD_1 src1_sel:DWORD
	v_and_b32_sdwa v2, v11, v213 dst_sel:DWORD dst_unused:UNUSED_PAD src0_sel:WORD_1 src1_sel:DWORD
	v_and_b32_sdwa v3, v10, v213 dst_sel:DWORD dst_unused:UNUSED_PAD src0_sel:WORD_1 src1_sel:DWORD
	v_add3_u32 v1, v1, v4, s76
	v_add3_u32 v0, v0, v5, s76
	v_add3_u32 v3, v10, v3, s76
	v_add3_u32 v2, v11, v2, s76
	v_and_b32_e32 v1, 0xffff0000, v1
	v_and_b32_e32 v0, 0xffff0000, v0
	v_or_b32_sdwa v1, v1, v2 dst_sel:DWORD dst_unused:UNUSED_PAD src0_sel:DWORD src1_sel:WORD_1
	v_or_b32_sdwa v0, v0, v3 dst_sel:DWORD dst_unused:UNUSED_PAD src0_sel:DWORD src1_sel:WORD_1
	ds_write_b64 v132, v[0:1] offset:4576
	s_waitcnt lgkmcnt(0)
	ds_read_b128 v[96:99], v133
	ds_read_b128 v[100:103], v133 offset:1088
	ds_read_b128 v[104:107], v133 offset:2176
	ds_read_b128 v[108:111], v133 offset:3264
	ds_read_b128 v[112:115], v133 offset:4352
	ds_read_b128 v[116:119], v133 offset:5440
	ds_read_b128 v[120:123], v133 offset:6528
	ds_read_b128 v[124:127], v133 offset:7616
	v_mov_b32_e32 v136, 0x4000
	v_mov_b32_e32 v137, 0
	s_waitcnt lgkmcnt(7)
	global_store_dwordx4 v[130:131], v[96:99], off
	v_lshl_add_u64 v[130:131], v[130:131], 0, v[136:137]
	s_waitcnt lgkmcnt(6)
	global_store_dwordx4 v[130:131], v[100:103], off
	v_lshl_add_u64 v[130:131], v[130:131], 0, v[136:137]
	s_waitcnt lgkmcnt(5)
	global_store_dwordx4 v[130:131], v[104:107], off
	v_lshl_add_u64 v[130:131], v[130:131], 0, v[136:137]
	s_waitcnt lgkmcnt(4)
	global_store_dwordx4 v[130:131], v[108:111], off
	v_lshl_add_u64 v[130:131], v[130:131], 0, v[136:137]
	s_waitcnt lgkmcnt(3)
	global_store_dwordx4 v[130:131], v[112:115], off
	v_lshl_add_u64 v[130:131], v[130:131], 0, v[136:137]
	s_waitcnt lgkmcnt(2)
	global_store_dwordx4 v[130:131], v[116:119], off
	v_lshl_add_u64 v[130:131], v[130:131], 0, v[136:137]
	s_waitcnt lgkmcnt(1)
	global_store_dwordx4 v[130:131], v[120:123], off
	v_lshl_add_u64 v[130:131], v[130:131], 0, v[136:137]
	s_waitcnt lgkmcnt(0)
	global_store_dwordx4 v[130:131], v[124:127], off
	s_cbranch_scc0 .LBB0_479

; __device__ __forceinline__ unsigned pk2(float lo, float hi) { return f2bf(lo) | (f2bf(hi) << 16); }
; __device__ __forceinline__ float rq_sum(float v) { v += __shfl_xor(v, 16); v += __shfl_xor(v, 32); return v; }
; __device__ __forceinline__ float frsq(float x) { return __builtin_amdgcn_rsqf(x); }
; __device__ __forceinline__ void ret_task(const Frame& F, int l, int task) {
;     ...
; #pragma unroll
;     for (int eb = 0; eb < 8; ++eb) g4[eb] = ld_f4(F.ret_g + l * 1024 + h * HD + eb * 16 + rq * 4);
; #pragma unroll
;     for (int qb = 0; qb < 2; ++qb) {
;         const int t = tq0 + qb * 16 + c;
;         float ss = 0.f;
; #pragma unroll
;         for (int eb = 0; eb < 8; ++eb) ss += (acc[qb][eb][0] * acc[qb][eb][0] + acc[qb][eb][1] * acc[qb][eb][1]) + (acc[qb][eb][2] * acc[qb][eb][2] + acc[qb][eb][3] * acc[qb][eb][3]);
;         const float rstd = frsq(rq_sum(ss) * (1.f / HD) + EPS);
; #pragma unroll
;         for (int eb = 0; eb < 8; ++eb) {
;             const int e0 = h * HD + eb * 16 + rq * 4;
;             const f32x4 gg = g4[eb]; const u32x2 gw = gwq[qb][eb];
;             u32x2 o; o.x = pk2(acc[qb][eb][0] * rstd * gg[0] * bf_lo(gw.x), acc[qb][eb][1] * rstd * gg[1] * bf_hi(gw.x));
;             o.y = pk2(acc[qb][eb][2] * rstd * gg[2] * bf_lo(gw.y), acc[qb][eb][3] * rstd * gg[3] * bf_hi(gw.y));
;             st_u2(MIX + (size_t)t * D + 1024 + e0, o);
;         }
.LBB0_633:
	s_lshl_b32 s0, s9, 2
	s_add_u32 s0, s2, s0
	s_addc_u32 s1, s3, 0
	v_ashrrev_i32_e32 v209, 31, v208
	v_lshl_add_u64 v[24:25], v[208:209], 2, s[0:1]
	global_load_dwordx4 v[20:23], v[24:25], off
	v_pk_mul_f32 v[58:59], v[90:91], v[90:91]
	v_pk_mul_f32 v[64:65], v[88:89], v[88:89]
	v_mul_f32_e32 v60, v84, v84
	v_mul_f32_e32 v62, v86, v86
	s_waitcnt vmcnt(17)
	v_pk_mov_b32 v[78:79], v[64:65], v[58:59] op_sel:[1,0]
	v_mov_b32_e32 v65, v59
	v_pk_fma_f32 v[58:59], v[84:85], v[84:85], v[60:61] op_sel_hi:[1,1,0]
	v_pk_fma_f32 v[82:83], v[86:87], v[86:87], v[62:63] op_sel_hi:[1,1,0]
	global_load_dwordx4 v[60:63], v[24:25], off offset:64
	v_mov_b32_e32 v52, v97
	v_mov_b32_e32 v53, v109
	v_mov_b32_e32 v56, v99
	v_mov_b32_e32 v57, v111
	v_mov_b32_e32 v26, v96
	v_mov_b32_e32 v27, v108
	v_mov_b32_e32 v54, v98
	v_mov_b32_e32 v55, v110
	v_pk_mul_f32 v[52:53], v[52:53], v[52:53]
	v_pk_mul_f32 v[56:57], v[56:57], v[56:57]
	v_pk_fma_f32 v[26:27], v[26:27], v[26:27], v[52:53]
	v_pk_fma_f32 v[52:53], v[54:55], v[54:55], v[56:57]
	v_pk_add_f32 v[54:55], v[78:79], v[64:65]
	v_pk_add_f32 v[26:27], v[26:27], v[52:53]
	v_pk_mul_f32 v[66:67], v[50:51], v[50:51]
	v_pk_mul_f32 v[72:73], v[48:49], v[48:49]
	v_pk_add_f32 v[52:53], v[54:55], v[54:55] op_sel_hi:[0,1]
	v_pk_add_f32 v[26:27], v[26:27], v[26:27] op_sel_hi:[0,1]
	v_pk_mov_b32 v[92:93], v[72:73], v[66:67] op_sel:[1,0]
	v_mov_b32_e32 v73, v67
	v_mul_f32_e32 v58, v68, v68
	v_mul_f32_e32 v82, v69, v69
	v_mul_f32_e32 v52, v70, v70
	v_mul_f32_e32 v26, v71, v71
	v_pk_add_f32 v[56:57], v[92:93], v[72:73]
	v_pk_add_f32 v[54:55], v[58:59], v[82:83]
	v_pk_add_f32 v[26:27], v[52:53], v[26:27]
	v_mul_f32_e32 v74, v44, v44
	v_mul_f32_e32 v76, v46, v46
	v_pk_add_f32 v[64:65], v[56:57], v[56:57] op_sel_hi:[0,1]
	global_load_dwordx4 v[56:59], v[24:25], off offset:128
	v_pk_add_f32 v[26:27], v[54:55], v[26:27]
	v_pk_fma_f32 v[66:67], v[44:45], v[44:45], v[74:75] op_sel_hi:[1,1,0]
	v_pk_fma_f32 v[74:75], v[46:47], v[46:47], v[76:77] op_sel_hi:[1,1,0]
	v_pk_add_f32 v[26:27], v[26:27], v[26:27] op_sel_hi:[0,1]
	v_mul_f32_e32 v66, v40, v40
	v_mul_f32_e32 v74, v41, v41
	v_mul_f32_e32 v64, v42, v42
	v_mul_f32_e32 v26, v43, v43
	v_pk_add_f32 v[66:67], v[66:67], v[74:75]
	v_pk_add_f32 v[26:27], v[64:65], v[26:27]
	global_load_dwordx4 v[76:79], v[24:25], off offset:192
	v_pk_add_f32 v[26:27], v[66:67], v[26:27]
	v_ashrrev_i32_e32 v197, 31, v196
	v_add_f32_e32 v26, v26, v27
	ds_bpermute_b32 v27, v226, v26
	v_mov_b32_e32 v80, v108
	v_mov_b32_e32 v81, v110
	v_mov_b32_e32 v110, v109
	s_waitcnt vmcnt(11)
	v_lshlrev_b32_e32 v83, 16, v207
	s_waitcnt lgkmcnt(0)
	v_add_f32_e32 v52, v26, v27
	ds_bpermute_b32 v53, v227, v52
	v_lshlrev_b64 v[26:27], 12, v[196:197]
	v_lshl_add_u64 v[100:101], s[62:63], 0, v[26:27]
	v_lshlrev_b32_e32 v82, 16, v206
	v_and_b32_e32 v95, 0xffff0000, v207
	s_waitcnt lgkmcnt(0)
	v_add_f32_e32 v26, v52, v53
	v_fmamk_f32 v26, v26, 0x3c000000, v214
	v_rsq_f32_e32 v92, v26
	global_load_dwordx4 v[72:75], v[24:25], off offset:256
	global_load_dwordx4 v[64:67], v[24:25], off offset:320
	global_load_dwordx4 v[52:55], v[24:25], off offset:384
	s_nop 0
	global_load_dwordx4 v[24:27], v[24:25], off offset:448
	v_and_b32_e32 v94, 0xffff0000, v206
	s_mov_b64 s[4:5], 0x26c00800
	v_pk_mul_f32 v[102:103], v[80:81], v[92:93] op_sel_hi:[1,0]
	v_pk_mul_f32 v[104:105], v[110:111], v[92:93] op_sel_hi:[1,0]
	s_mov_b32 s0, 0x26c00000
	v_ashrrev_i32_e32 v195, 31, v194
	s_add_i32 s8, s8, s82
	s_cmpk_gt_i32 s8, 0xfff
	s_waitcnt vmcnt(7)
	v_mov_b32_e32 v80, v20
	v_mov_b32_e32 v81, v22
	v_mov_b32_e32 v22, v21
	v_pk_mul_f32 v[20:21], v[80:81], v[102:103]
	v_pk_mul_f32 v[102:103], v[22:23], v[104:105]
	v_pk_mul_f32 v[20:21], v[20:21], v[82:83]
	v_pk_mul_f32 v[82:83], v[102:103], v[94:95]
	v_and_b32_sdwa v93, v21, v213 dst_sel:DWORD dst_unused:UNUSED_PAD src0_sel:WORD_1 src1_sel:DWORD
	v_and_b32_sdwa v94, v20, v213 dst_sel:DWORD dst_unused:UNUSED_PAD src0_sel:WORD_1 src1_sel:DWORD
	v_add3_u32 v20, v20, v94, s76
	v_add3_u32 v21, v21, v93, s76
	v_and_b32_sdwa v93, v83, v213 dst_sel:DWORD dst_unused:UNUSED_PAD src0_sel:WORD_1 src1_sel:DWORD
	v_and_b32_sdwa v94, v82, v213 dst_sel:DWORD dst_unused:UNUSED_PAD src0_sel:WORD_1 src1_sel:DWORD
	v_add3_u32 v83, v83, v93, s76
	v_add3_u32 v82, v82, v94, s76
	v_and_b32_e32 v83, 0xffff0000, v83
	v_and_b32_e32 v82, 0xffff0000, v82
	v_lshl_add_u64 v[94:95], v[100:101], 0, v[156:157]
	v_and_b32_e32 v128, 15, v211
	v_lshrrev_b32_e32 v129, 4, v211
	v_lshrrev_b32_e32 v134, 6, v212
	v_mul_u32_u24_e32 v134, 0x2200, v134
	v_mul_u32_u24_e32 v135, 0x110, v128
	v_add_u32_e32 v132, v134, v135
	v_lshl_add_u32 v132, v129, 3, v132
	v_mul_u32_u24_e32 v135, 0x110, v129
	v_add_u32_e32 v133, v134, v135
	v_lshl_add_u32 v133, v128, 4, v133
	v_mul_u32_u24_e32 v135, 0xff8, v129
	v_mul_u32_u24_e32 v136, 0xff0, v128
	v_sub_u32_e32 v136, v135, v136
	v_ashrrev_i32_e32 v137, 31, v136
	v_lshl_add_u64 v[130:131], v[94:95], 0, s[4:5]
	v_lshl_add_u64 v[130:131], v[130:131], 0, v[136:137]
	v_or_b32_sdwa v21, v83, v21 dst_sel:DWORD dst_unused:UNUSED_PAD src0_sel:DWORD src1_sel:WORD_1
	v_or_b32_sdwa v20, v82, v20 dst_sel:DWORD dst_unused:UNUSED_PAD src0_sel:DWORD src1_sel:WORD_1
	v_lshl_add_u64 v[82:83], v[94:95], 0, s[4:5]
	v_add_co_u32_e32 v94, vcc, s0, v94
	v_lshlrev_b32_e32 v101, 16, v205
	s_nop 0
	v_addc_co_u32_e32 v95, vcc, 0, v95, vcc
	ds_write_b64 v132, v[20:21]
	v_mov_b32_e32 v20, v96
	v_mov_b32_e32 v21, v98
	v_pk_mul_f32 v[94:95], v[20:21], v[92:93] op_sel_hi:[1,0]
	s_waitcnt vmcnt(6)
; __device__ __forceinline__ unsigned pk2(float lo, float hi) { return f2bf(lo) | (f2bf(hi) << 16); }
; __device__ __forceinline__ float rq_sum(float v) { v += __shfl_xor(v, 16); v += __shfl_xor(v, 32); return v; }
; __device__ __forceinline__ float frsq(float x) { return __builtin_amdgcn_rsqf(x); }
; __device__ __forceinline__ void ret_task(const Frame& F, int l, int task) {
;     ...
;     for (int qb = 0; qb < 2; ++qb) {
;         const int t = tq0 + qb * 16 + c;
;         float ss = 0.f;
; #pragma unroll
;         for (int eb = 0; eb < 8; ++eb) ss += (acc[qb][eb][0] * acc[qb][eb][0] + acc[qb][eb][1] * acc[qb][eb][1]) + (acc[qb][eb][2] * acc[qb][eb][2] + acc[qb][eb][3] * acc[qb][eb][3]);
;         const float rstd = frsq(rq_sum(ss) * (1.f / HD) + EPS);
; #pragma unroll
;         for (int eb = 0; eb < 8; ++eb) {
;             const int e0 = h * HD + eb * 16 + rq * 4;
;             const f32x4 gg = g4[eb]; const u32x2 gw = gwq[qb][eb];
;             u32x2 o; o.x = pk2(acc[qb][eb][0] * rstd * gg[0] * bf_lo(gw.x), acc[qb][eb][1] * rstd * gg[1] * bf_hi(gw.x));
;             o.y = pk2(acc[qb][eb][2] * rstd * gg[2] * bf_lo(gw.y), acc[qb][eb][3] * rstd * gg[3] * bf_hi(gw.y));
;             st_u2(MIX + (size_t)t * D + 1024 + e0, o);
;         }
	v_mov_b32_e32 v20, v60
	v_mov_b32_e32 v21, v62
	v_mov_b32_e32 v98, v97
	v_pk_mul_f32 v[94:95], v[20:21], v[94:95]
	v_lshlrev_b32_e32 v100, 16, v204
	v_pk_mul_f32 v[96:97], v[98:99], v[92:93] op_sel_hi:[1,0]
	v_mov_b32_e32 v62, v61
	v_pk_mul_f32 v[94:95], v[94:95], v[100:101]
	v_pk_mul_f32 v[60:61], v[62:63], v[96:97]
	v_and_b32_e32 v97, 0xffff0000, v205
	v_and_b32_e32 v96, 0xffff0000, v204
	v_pk_mul_f32 v[60:61], v[60:61], v[96:97]
	v_and_b32_sdwa v93, v95, v213 dst_sel:DWORD dst_unused:UNUSED_PAD src0_sel:WORD_1 src1_sel:DWORD
	v_and_b32_sdwa v96, v94, v213 dst_sel:DWORD dst_unused:UNUSED_PAD src0_sel:WORD_1 src1_sel:DWORD
	v_add3_u32 v94, v94, v96, s76
	v_add3_u32 v93, v95, v93, s76
	v_and_b32_sdwa v95, v61, v213 dst_sel:DWORD dst_unused:UNUSED_PAD src0_sel:WORD_1 src1_sel:DWORD
	v_and_b32_sdwa v96, v60, v213 dst_sel:DWORD dst_unused:UNUSED_PAD src0_sel:WORD_1 src1_sel:DWORD
	v_add3_u32 v61, v61, v95, s76
	v_add3_u32 v60, v60, v96, s76
	v_and_b32_e32 v61, 0xffff0000, v61
	v_and_b32_e32 v60, 0xffff0000, v60
	v_or_b32_sdwa v61, v61, v93 dst_sel:DWORD dst_unused:UNUSED_PAD src0_sel:DWORD src1_sel:WORD_1
	v_or_b32_sdwa v60, v60, v94 dst_sel:DWORD dst_unused:UNUSED_PAD src0_sel:DWORD src1_sel:WORD_1
	ds_write_b64 v132, v[60:61] offset:32
	v_mov_b32_e32 v60, v88
	v_mov_b32_e32 v61, v90
	v_mov_b32_e32 v90, v89
	v_pk_mul_f32 v[94:95], v[60:61], v[92:93] op_sel_hi:[1,0]
	s_waitcnt vmcnt(5)
	v_mov_b32_e32 v61, v58
	v_pk_mul_f32 v[88:89], v[90:91], v[92:93] op_sel_hi:[1,0]
	v_mov_b32_e32 v58, v57
	v_mov_b32_e32 v60, v56
	v_pk_mul_f32 v[56:57], v[58:59], v[88:89]
	v_and_b32_e32 v89, 0xffff0000, v203
	v_and_b32_e32 v88, 0xffff0000, v202
	v_pk_mul_f32 v[94:95], v[60:61], v[94:95]
	v_lshlrev_b32_e32 v97, 16, v203
	v_lshlrev_b32_e32 v96, 16, v202
	v_pk_mul_f32 v[56:57], v[56:57], v[88:89]
	v_pk_mul_f32 v[94:95], v[94:95], v[96:97]
	v_and_b32_sdwa v90, v57, v213 dst_sel:DWORD dst_unused:UNUSED_PAD src0_sel:WORD_1 src1_sel:DWORD
	v_and_b32_sdwa v91, v56, v213 dst_sel:DWORD dst_unused:UNUSED_PAD src0_sel:WORD_1 src1_sel:DWORD
	v_and_b32_sdwa v88, v95, v213 dst_sel:DWORD dst_unused:UNUSED_PAD src0_sel:WORD_1 src1_sel:DWORD
	v_and_b32_sdwa v89, v94, v213 dst_sel:DWORD dst_unused:UNUSED_PAD src0_sel:WORD_1 src1_sel:DWORD
	v_add3_u32 v57, v57, v90, s76
	v_add3_u32 v56, v56, v91, s76
	v_add3_u32 v89, v94, v89, s76
	v_add3_u32 v88, v95, v88, s76
	v_and_b32_e32 v57, 0xffff0000, v57
	v_and_b32_e32 v56, 0xffff0000, v56
	v_or_b32_sdwa v57, v57, v88 dst_sel:DWORD dst_unused:UNUSED_PAD src0_sel:DWORD src1_sel:WORD_1
	v_or_b32_sdwa v56, v56, v89 dst_sel:DWORD dst_unused:UNUSED_PAD src0_sel:DWORD src1_sel:WORD_1
	ds_write_b64 v132, v[56:57] offset:64
	v_mov_b32_e32 v56, v84
	v_mov_b32_e32 v57, v86
	v_mov_b32_e32 v86, v85
	v_pk_mul_f32 v[88:89], v[56:57], v[92:93] op_sel_hi:[1,0]
	s_waitcnt vmcnt(4)
	v_mov_b32_e32 v57, v78
	v_pk_mul_f32 v[84:85], v[86:87], v[92:93] op_sel_hi:[1,0]
	v_mov_b32_e32 v78, v77
	v_mov_b32_e32 v56, v76
	v_pk_mul_f32 v[76:77], v[78:79], v[84:85]
	v_and_b32_e32 v85, 0xffff0000, v201
	v_and_b32_e32 v84, 0xffff0000, v200
	v_pk_mul_f32 v[88:89], v[56:57], v[88:89]
	v_lshlrev_b32_e32 v91, 16, v201
	v_lshlrev_b32_e32 v90, 16, v200
	v_pk_mul_f32 v[76:77], v[76:77], v[84:85]
	v_pk_mul_f32 v[88:89], v[88:89], v[90:91]
	v_and_b32_sdwa v86, v77, v213 dst_sel:DWORD dst_unused:UNUSED_PAD src0_sel:WORD_1 src1_sel:DWORD
	v_and_b32_sdwa v87, v76, v213 dst_sel:DWORD dst_unused:UNUSED_PAD src0_sel:WORD_1 src1_sel:DWORD
	v_and_b32_sdwa v84, v89, v213 dst_sel:DWORD dst_unused:UNUSED_PAD src0_sel:WORD_1 src1_sel:DWORD
	v_and_b32_sdwa v85, v88, v213 dst_sel:DWORD dst_unused:UNUSED_PAD src0_sel:WORD_1 src1_sel:DWORD
	v_add3_u32 v77, v77, v86, s76
	v_add3_u32 v76, v76, v87, s76
	v_add3_u32 v85, v88, v85, s76
	v_add3_u32 v84, v89, v84, s76
	v_and_b32_e32 v77, 0xffff0000, v77
	v_and_b32_e32 v76, 0xffff0000, v76
	v_or_b32_sdwa v77, v77, v84 dst_sel:DWORD dst_unused:UNUSED_PAD src0_sel:DWORD src1_sel:WORD_1
	v_or_b32_sdwa v76, v76, v85 dst_sel:DWORD dst_unused:UNUSED_PAD src0_sel:DWORD src1_sel:WORD_1
	ds_write_b64 v132, v[76:77] offset:96
	v_mov_b32_e32 v76, v68
	v_mov_b32_e32 v77, v70
	v_mov_b32_e32 v70, v69
	v_pk_mul_f32 v[84:85], v[76:77], v[92:93] op_sel_hi:[1,0]
	s_waitcnt vmcnt(3)
	v_mov_b32_e32 v77, v74
	v_pk_mul_f32 v[68:69], v[70:71], v[92:93] op_sel_hi:[1,0]
	v_mov_b32_e32 v74, v73
	v_mov_b32_e32 v76, v72
	v_pk_mul_f32 v[68:69], v[74:75], v[68:69]
	v_and_b32_e32 v71, 0xffff0000, v199
	v_and_b32_e32 v70, 0xffff0000, v198
	v_pk_mul_f32 v[84:85], v[76:77], v[84:85]
	v_lshlrev_b32_e32 v87, 16, v199
	v_lshlrev_b32_e32 v86, 16, v198
	v_pk_mul_f32 v[68:69], v[68:69], v[70:71]
	v_pk_mul_f32 v[84:85], v[84:85], v[86:87]
	v_and_b32_sdwa v72, v69, v213 dst_sel:DWORD dst_unused:UNUSED_PAD src0_sel:WORD_1 src1_sel:DWORD
	v_and_b32_sdwa v73, v68, v213 dst_sel:DWORD dst_unused:UNUSED_PAD src0_sel:WORD_1 src1_sel:DWORD
	v_and_b32_sdwa v70, v85, v213 dst_sel:DWORD dst_unused:UNUSED_PAD src0_sel:WORD_1 src1_sel:DWORD
	v_and_b32_sdwa v71, v84, v213 dst_sel:DWORD dst_unused:UNUSED_PAD src0_sel:WORD_1 src1_sel:DWORD
	v_add3_u32 v69, v69, v72, s76
	v_add3_u32 v68, v68, v73, s76
	v_add3_u32 v71, v84, v71, s76
	v_add3_u32 v70, v85, v70, s76
	v_and_b32_e32 v69, 0xffff0000, v69
	v_and_b32_e32 v68, 0xffff0000, v68
	v_or_b32_sdwa v69, v69, v70 dst_sel:DWORD dst_unused:UNUSED_PAD src0_sel:DWORD src1_sel:WORD_1
	v_or_b32_sdwa v68, v68, v71 dst_sel:DWORD dst_unused:UNUSED_PAD src0_sel:DWORD src1_sel:WORD_1
	ds_write_b64 v132, v[68:69] offset:128
	v_mov_b32_e32 v68, v48
	v_mov_b32_e32 v69, v50
	v_mov_b32_e32 v50, v49
	v_pk_mul_f32 v[70:71], v[68:69], v[92:93] op_sel_hi:[1,0]
	s_waitcnt vmcnt(2)
; __device__ __forceinline__ unsigned pk2(float lo, float hi) { return f2bf(lo) | (f2bf(hi) << 16); }
; __device__ __forceinline__ float rq_sum(float v) { v += __shfl_xor(v, 16); v += __shfl_xor(v, 32); return v; }
; __device__ __forceinline__ float frsq(float x) { return __builtin_amdgcn_rsqf(x); }
; __device__ __forceinline__ void ret_task(const Frame& F, int l, int task) {
;     ...
;     for (int qb = 0; qb < 2; ++qb) {
;         const int t = tq0 + qb * 16 + c;
;         float ss = 0.f;
; #pragma unroll
;         for (int eb = 0; eb < 8; ++eb) ss += (acc[qb][eb][0] * acc[qb][eb][0] + acc[qb][eb][1] * acc[qb][eb][1]) + (acc[qb][eb][2] * acc[qb][eb][2] + acc[qb][eb][3] * acc[qb][eb][3]);
;         const float rstd = frsq(rq_sum(ss) * (1.f / HD) + EPS);
; #pragma unroll
;         for (int eb = 0; eb < 8; ++eb) {
;             const int e0 = h * HD + eb * 16 + rq * 4;
;             const f32x4 gg = g4[eb]; const u32x2 gw = gwq[qb][eb];
;             u32x2 o; o.x = pk2(acc[qb][eb][0] * rstd * gg[0] * bf_lo(gw.x), acc[qb][eb][1] * rstd * gg[1] * bf_hi(gw.x));
;             o.y = pk2(acc[qb][eb][2] * rstd * gg[2] * bf_lo(gw.y), acc[qb][eb][3] * rstd * gg[3] * bf_hi(gw.y));
;             st_u2(MIX + (size_t)t * D + 1024 + e0, o);
;         }
	v_mov_b32_e32 v69, v66
	v_pk_mul_f32 v[48:49], v[50:51], v[92:93] op_sel_hi:[1,0]
	v_mov_b32_e32 v66, v65
	v_mov_b32_e32 v68, v64
	v_pk_mul_f32 v[48:49], v[66:67], v[48:49]
	v_and_b32_e32 v51, 0xffff0000, v167
	v_and_b32_e32 v50, 0xffff0000, v166
	v_pk_mul_f32 v[70:71], v[68:69], v[70:71]
	v_lshlrev_b32_e32 v73, 16, v167
	v_lshlrev_b32_e32 v72, 16, v166
	v_pk_mul_f32 v[48:49], v[48:49], v[50:51]
	v_pk_mul_f32 v[70:71], v[70:71], v[72:73]
	v_and_b32_sdwa v64, v49, v213 dst_sel:DWORD dst_unused:UNUSED_PAD src0_sel:WORD_1 src1_sel:DWORD
	v_and_b32_sdwa v65, v48, v213 dst_sel:DWORD dst_unused:UNUSED_PAD src0_sel:WORD_1 src1_sel:DWORD
	v_and_b32_sdwa v50, v71, v213 dst_sel:DWORD dst_unused:UNUSED_PAD src0_sel:WORD_1 src1_sel:DWORD
	v_and_b32_sdwa v51, v70, v213 dst_sel:DWORD dst_unused:UNUSED_PAD src0_sel:WORD_1 src1_sel:DWORD
	v_add3_u32 v49, v49, v64, s76
	v_add3_u32 v48, v48, v65, s76
	v_add3_u32 v51, v70, v51, s76
	v_add3_u32 v50, v71, v50, s76
	v_and_b32_e32 v49, 0xffff0000, v49
	v_and_b32_e32 v48, 0xffff0000, v48
	v_or_b32_sdwa v49, v49, v50 dst_sel:DWORD dst_unused:UNUSED_PAD src0_sel:DWORD src1_sel:WORD_1
	v_or_b32_sdwa v48, v48, v51 dst_sel:DWORD dst_unused:UNUSED_PAD src0_sel:DWORD src1_sel:WORD_1
	ds_write_b64 v132, v[48:49] offset:160
	v_mov_b32_e32 v48, v44
	v_mov_b32_e32 v49, v46
	v_pk_mul_f32 v[50:51], v[48:49], v[92:93] op_sel_hi:[1,0]
	s_waitcnt vmcnt(1)
	v_mov_b32_e32 v48, v52
	v_mov_b32_e32 v49, v54
	v_mov_b32_e32 v46, v45
	v_pk_mul_f32 v[50:51], v[48:49], v[50:51]
	v_lshlrev_b32_e32 v65, 16, v165
	v_lshlrev_b32_e32 v64, 16, v164
	v_pk_mul_f32 v[44:45], v[46:47], v[92:93] op_sel_hi:[1,0]
	v_mov_b32_e32 v54, v53
	v_pk_mul_f32 v[50:51], v[50:51], v[64:65]
	v_pk_mul_f32 v[44:45], v[54:55], v[44:45]
	v_and_b32_e32 v47, 0xffff0000, v165
	v_and_b32_e32 v46, 0xffff0000, v164
	v_pk_mul_f32 v[44:45], v[44:45], v[46:47]
	v_and_b32_sdwa v46, v51, v213 dst_sel:DWORD dst_unused:UNUSED_PAD src0_sel:WORD_1 src1_sel:DWORD
	v_and_b32_sdwa v47, v50, v213 dst_sel:DWORD dst_unused:UNUSED_PAD src0_sel:WORD_1 src1_sel:DWORD
	v_add3_u32 v47, v50, v47, s76
	v_add3_u32 v46, v51, v46, s76
	v_and_b32_sdwa v50, v45, v213 dst_sel:DWORD dst_unused:UNUSED_PAD src0_sel:WORD_1 src1_sel:DWORD
	v_and_b32_sdwa v51, v44, v213 dst_sel:DWORD dst_unused:UNUSED_PAD src0_sel:WORD_1 src1_sel:DWORD
	v_add3_u32 v45, v45, v50, s76
	v_add3_u32 v44, v44, v51, s76
	v_and_b32_e32 v45, 0xffff0000, v45
	v_and_b32_e32 v44, 0xffff0000, v44
	v_or_b32_sdwa v45, v45, v46 dst_sel:DWORD dst_unused:UNUSED_PAD src0_sel:DWORD src1_sel:WORD_1
	v_or_b32_sdwa v44, v44, v47 dst_sel:DWORD dst_unused:UNUSED_PAD src0_sel:DWORD src1_sel:WORD_1
	ds_write_b64 v132, v[44:45] offset:192
	v_mov_b32_e32 v44, v40
	v_mov_b32_e32 v45, v42
	v_pk_mul_f32 v[46:47], v[44:45], v[92:93] op_sel_hi:[1,0]
	s_waitcnt vmcnt(0)
	v_mov_b32_e32 v44, v24
	v_mov_b32_e32 v45, v26
	v_mov_b32_e32 v42, v41
	v_pk_mul_f32 v[46:47], v[44:45], v[46:47]
	v_lshlrev_b32_e32 v51, 16, v163
	v_lshlrev_b32_e32 v50, 16, v162
	v_pk_mul_f32 v[40:41], v[42:43], v[92:93] op_sel_hi:[1,0]
	v_mov_b32_e32 v26, v25
	v_pk_mul_f32 v[46:47], v[46:47], v[50:51]
	v_pk_mul_f32 v[24:25], v[26:27], v[40:41]
	v_and_b32_e32 v41, 0xffff0000, v163
	v_and_b32_e32 v40, 0xffff0000, v162
	v_pk_mul_f32 v[24:25], v[24:25], v[40:41]
	v_and_b32_sdwa v40, v47, v213 dst_sel:DWORD dst_unused:UNUSED_PAD src0_sel:WORD_1 src1_sel:DWORD
	v_and_b32_sdwa v41, v46, v213 dst_sel:DWORD dst_unused:UNUSED_PAD src0_sel:WORD_1 src1_sel:DWORD
	v_mov_b32_e32 v42, v37
	v_mov_b32_e32 v43, v33
	v_add3_u32 v52, v46, v41, s76
	v_add3_u32 v53, v47, v40, s76
	v_mov_b32_e32 v40, v36
	v_mov_b32_e32 v41, v32
	v_pk_mul_f32 v[42:43], v[42:43], v[42:43]
	v_mov_b32_e32 v46, v39
	v_mov_b32_e32 v47, v35
	v_pk_fma_f32 v[40:41], v[40:41], v[40:41], v[42:43]
	v_mov_b32_e32 v42, v38
	v_mov_b32_e32 v43, v34
	v_pk_mul_f32 v[46:47], v[46:47], v[46:47]
	v_and_b32_sdwa v64, v25, v213 dst_sel:DWORD dst_unused:UNUSED_PAD src0_sel:WORD_1 src1_sel:DWORD
	v_pk_fma_f32 v[42:43], v[42:43], v[42:43], v[46:47]
	v_pk_mul_f32 v[46:47], v[28:29], v[28:29]
	v_pk_add_f32 v[40:41], v[40:41], v[42:43]
	v_pk_mul_f32 v[42:43], v[30:31], v[30:31]
	v_pk_add_f32 v[40:41], v[40:41], v[40:41] op_sel:[0,1] op_sel_hi:[1,0]
	v_pk_mov_b32 v[50:51], v[46:47], v[42:43] op_sel:[1,0]
	v_mov_b32_e32 v47, v43
	v_pk_add_f32 v[42:43], v[50:51], v[46:47]
	v_mul_f32_e32 v46, v12, v12
	v_mul_f32_e32 v47, v13, v13
	v_pk_add_f32 v[42:43], v[42:43], v[42:43] op_sel:[0,1] op_sel_hi:[1,0]
	v_mov_b32_e32 v41, v46
	v_mov_b32_e32 v43, v47
	v_pk_add_f32 v[40:41], v[40:41], v[42:43]
	v_mul_f32_e32 v42, v17, v17
	v_mul_f32_e32 v46, v19, v19
	v_mul_f32_e32 v50, v14, v14
	v_mul_f32_e32 v51, v15, v15
	v_pk_fma_f32 v[42:43], v[16:17], v[16:17], v[42:43] op_sel_hi:[1,1,0]
	v_pk_fma_f32 v[46:47], v[18:19], v[18:19], v[46:47] op_sel_hi:[1,1,0]
	v_mov_b32_e32 v43, v50
	v_mov_b32_e32 v47, v51
	v_pk_add_f32 v[42:43], v[42:43], v[46:47]
	v_pk_mul_f32 v[46:47], v[8:9], v[8:9]
	v_pk_add_f32 v[40:41], v[40:41], v[42:43]
	v_pk_mul_f32 v[42:43], v[10:11], v[10:11]
	v_pk_add_f32 v[40:41], v[40:41], v[40:41] op_sel:[0,1] op_sel_hi:[1,0]
	v_pk_mov_b32 v[50:51], v[46:47], v[42:43] op_sel:[1,0]
	v_mov_b32_e32 v47, v43
	v_pk_add_f32 v[42:43], v[50:51], v[46:47]
	v_mul_f32_e32 v46, v0, v0
	v_mul_f32_e32 v47, v1, v1
	v_pk_add_f32 v[42:43], v[42:43], v[42:43] op_sel:[0,1] op_sel_hi:[1,0]
	v_mov_b32_e32 v41, v46
	v_mov_b32_e32 v43, v47
	v_pk_add_f32 v[40:41], v[40:41], v[42:43]
	v_mul_f32_e32 v42, v5, v5
	v_mul_f32_e32 v46, v7, v7
	v_mul_f32_e32 v50, v2, v2
	v_mul_f32_e32 v51, v3, v3
	v_pk_fma_f32 v[42:43], v[4:5], v[4:5], v[42:43] op_sel_hi:[1,1,0]
	v_pk_fma_f32 v[46:47], v[6:7], v[6:7], v[46:47] op_sel_hi:[1,1,0]
	v_mov_b32_e32 v43, v50
	v_mov_b32_e32 v47, v51
	v_pk_add_f32 v[42:43], v[42:43], v[46:47]
	v_add3_u32 v25, v25, v64, s76
	v_pk_add_f32 v[40:41], v[40:41], v[42:43]
	v_and_b32_sdwa v42, v24, v213 dst_sel:DWORD dst_unused:UNUSED_PAD src0_sel:WORD_1 src1_sel:DWORD
	v_add_f32_e32 v40, v40, v41
	ds_bpermute_b32 v41, v226, v40
	v_add3_u32 v24, v24, v42, s76
	v_and_b32_e32 v25, 0xffff0000, v25
	v_and_b32_e32 v24, 0xffff0000, v24
	v_or_b32_sdwa v25, v25, v53 dst_sel:DWORD dst_unused:UNUSED_PAD src0_sel:DWORD src1_sel:WORD_1
	s_waitcnt lgkmcnt(0)
; __device__ __forceinline__ unsigned pk2(float lo, float hi) { return f2bf(lo) | (f2bf(hi) << 16); }
; __device__ __forceinline__ float rq_sum(float v) { v += __shfl_xor(v, 16); v += __shfl_xor(v, 32); return v; }
; __device__ __forceinline__ float frsq(float x) { return __builtin_amdgcn_rsqf(x); }
; __device__ __forceinline__ void ret_task(const Frame& F, int l, int task) {
;     ...
;     for (int qb = 0; qb < 2; ++qb) {
;         const int t = tq0 + qb * 16 + c;
;         float ss = 0.f;
; #pragma unroll
;         for (int eb = 0; eb < 8; ++eb) ss += (acc[qb][eb][0] * acc[qb][eb][0] + acc[qb][eb][1] * acc[qb][eb][1]) + (acc[qb][eb][2] * acc[qb][eb][2] + acc[qb][eb][3] * acc[qb][eb][3]);
;         const float rstd = frsq(rq_sum(ss) * (1.f / HD) + EPS);
; #pragma unroll
;         for (int eb = 0; eb < 8; ++eb) {
;             const int e0 = h * HD + eb * 16 + rq * 4;
;             const f32x4 gg = g4[eb]; const u32x2 gw = gwq[qb][eb];
;             u32x2 o; o.x = pk2(acc[qb][eb][0] * rstd * gg[0] * bf_lo(gw.x), acc[qb][eb][1] * rstd * gg[1] * bf_hi(gw.x));
;             o.y = pk2(acc[qb][eb][2] * rstd * gg[2] * bf_lo(gw.y), acc[qb][eb][3] * rstd * gg[3] * bf_hi(gw.y));
;             st_u2(MIX + (size_t)t * D + 1024 + e0, o);
;         }
	v_add_f32_e32 v40, v40, v41
	ds_bpermute_b32 v41, v227, v40
	v_or_b32_sdwa v24, v24, v52 dst_sel:DWORD dst_unused:UNUSED_PAD src0_sel:DWORD src1_sel:WORD_1
	ds_write_b64 v132, v[24:25] offset:224
	v_mov_b32_e32 v43, v38
	v_mov_b32_e32 v38, v37
	s_waitcnt lgkmcnt(0)
	v_add_f32_e32 v24, v40, v41
	v_fmamk_f32 v24, v24, 0x3c000000, v214
	v_rsq_f32_e32 v24, v24
	v_mov_b32_e32 v42, v36
	v_lshlrev_b32_e32 v47, 16, v161
	v_lshlrev_b32_e32 v46, 16, v160
	v_pk_mul_f32 v[36:37], v[38:39], v[24:25] op_sel_hi:[1,0]
	v_pk_mul_f32 v[42:43], v[42:43], v[24:25] op_sel_hi:[1,0]
	v_pk_mul_f32 v[22:23], v[22:23], v[36:37]
	v_and_b32_e32 v37, 0xffff0000, v161
	v_and_b32_e32 v36, 0xffff0000, v160
	v_pk_mul_f32 v[42:43], v[80:81], v[42:43]
	v_pk_mul_f32 v[22:23], v[22:23], v[36:37]
	v_pk_mul_f32 v[42:43], v[42:43], v[46:47]
	v_and_b32_sdwa v38, v22, v213 dst_sel:DWORD dst_unused:UNUSED_PAD src0_sel:WORD_1 src1_sel:DWORD
	v_lshlrev_b64 v[40:41], 12, v[194:195]
	v_and_b32_sdwa v36, v42, v213 dst_sel:DWORD dst_unused:UNUSED_PAD src0_sel:WORD_1 src1_sel:DWORD
	v_add3_u32 v22, v22, v38, s76
	v_lshl_add_u64 v[40:41], s[62:63], 0, v[40:41]
	v_add3_u32 v36, v42, v36, s76
	v_and_b32_sdwa v37, v23, v213 dst_sel:DWORD dst_unused:UNUSED_PAD src0_sel:WORD_1 src1_sel:DWORD
	v_and_b32_e32 v22, 0xffff0000, v22
	v_and_b32_sdwa v25, v43, v213 dst_sel:DWORD dst_unused:UNUSED_PAD src0_sel:WORD_1 src1_sel:DWORD
	v_add3_u32 v23, v23, v37, s76
	v_or_b32_sdwa v22, v22, v36 dst_sel:DWORD dst_unused:UNUSED_PAD src0_sel:DWORD src1_sel:WORD_1
	v_lshl_add_u64 v[36:37], v[40:41], 0, v[156:157]
	v_add3_u32 v25, v43, v25, s76
	v_and_b32_e32 v23, 0xffff0000, v23
	v_lshl_add_u64 v[38:39], v[36:37], 0, s[4:5]
	v_add_co_u32_e32 v36, vcc, s0, v36
	v_or_b32_sdwa v23, v23, v25 dst_sel:DWORD dst_unused:UNUSED_PAD src0_sel:DWORD src1_sel:WORD_1
	s_nop 0
	v_addc_co_u32_e32 v37, vcc, 0, v37, vcc
	ds_write_b64 v132, v[22:23] offset:4352
	v_mov_b32_e32 v22, v32
	v_mov_b32_e32 v23, v34
	v_pk_mul_f32 v[22:23], v[22:23], v[24:25] op_sel_hi:[1,0]
	v_mov_b32_e32 v34, v33
	v_pk_mul_f32 v[20:21], v[20:21], v[22:23]
	v_lshlrev_b32_e32 v23, 16, v159
	v_lshlrev_b32_e32 v22, 16, v158
	v_pk_mul_f32 v[20:21], v[20:21], v[22:23]
	v_pk_mul_f32 v[22:23], v[34:35], v[24:25] op_sel_hi:[1,0]
	v_and_b32_e32 v33, 0xffff0000, v159
	v_pk_mul_f32 v[22:23], v[62:63], v[22:23]
	v_and_b32_e32 v32, 0xffff0000, v158
	v_pk_mul_f32 v[22:23], v[22:23], v[32:33]
	v_and_b32_sdwa v25, v21, v213 dst_sel:DWORD dst_unused:UNUSED_PAD src0_sel:WORD_1 src1_sel:DWORD
	v_and_b32_sdwa v32, v20, v213 dst_sel:DWORD dst_unused:UNUSED_PAD src0_sel:WORD_1 src1_sel:DWORD
	v_add3_u32 v20, v20, v32, s76
	v_add3_u32 v21, v21, v25, s76
	v_and_b32_sdwa v25, v23, v213 dst_sel:DWORD dst_unused:UNUSED_PAD src0_sel:WORD_1 src1_sel:DWORD
	v_and_b32_sdwa v32, v22, v213 dst_sel:DWORD dst_unused:UNUSED_PAD src0_sel:WORD_1 src1_sel:DWORD
	v_add3_u32 v23, v23, v25, s76
	v_add3_u32 v22, v22, v32, s76
	v_and_b32_e32 v23, 0xffff0000, v23
	v_and_b32_e32 v22, 0xffff0000, v22
	v_or_b32_sdwa v21, v23, v21 dst_sel:DWORD dst_unused:UNUSED_PAD src0_sel:DWORD src1_sel:WORD_1
	v_or_b32_sdwa v20, v22, v20 dst_sel:DWORD dst_unused:UNUSED_PAD src0_sel:DWORD src1_sel:WORD_1
	ds_write_b64 v132, v[20:21] offset:4384
	v_mov_b32_e32 v20, v28
	v_mov_b32_e32 v21, v30
	v_pk_mul_f32 v[20:21], v[20:21], v[24:25] op_sel_hi:[1,0]
	v_lshlrev_b32_e32 v23, 16, v155
	v_pk_mul_f32 v[20:21], v[60:61], v[20:21]
	v_lshlrev_b32_e32 v22, 16, v154
	v_mov_b32_e32 v30, v29
	v_pk_mul_f32 v[20:21], v[20:21], v[22:23]
	v_pk_mul_f32 v[22:23], v[30:31], v[24:25] op_sel_hi:[1,0]
	v_and_b32_e32 v29, 0xffff0000, v155
	v_pk_mul_f32 v[22:23], v[58:59], v[22:23]
	v_and_b32_e32 v28, 0xffff0000, v154
	v_pk_mul_f32 v[22:23], v[22:23], v[28:29]
	v_and_b32_sdwa v25, v21, v213 dst_sel:DWORD dst_unused:UNUSED_PAD src0_sel:WORD_1 src1_sel:DWORD
	v_and_b32_sdwa v28, v20, v213 dst_sel:DWORD dst_unused:UNUSED_PAD src0_sel:WORD_1 src1_sel:DWORD
	v_add3_u32 v20, v20, v28, s76
	v_add3_u32 v21, v21, v25, s76
	v_and_b32_sdwa v25, v23, v213 dst_sel:DWORD dst_unused:UNUSED_PAD src0_sel:WORD_1 src1_sel:DWORD
	v_and_b32_sdwa v28, v22, v213 dst_sel:DWORD dst_unused:UNUSED_PAD src0_sel:WORD_1 src1_sel:DWORD
	v_add3_u32 v23, v23, v25, s76
	v_add3_u32 v22, v22, v28, s76
	v_and_b32_e32 v23, 0xffff0000, v23
	v_and_b32_e32 v22, 0xffff0000, v22
	v_or_b32_sdwa v21, v23, v21 dst_sel:DWORD dst_unused:UNUSED_PAD src0_sel:DWORD src1_sel:WORD_1
	v_or_b32_sdwa v20, v22, v20 dst_sel:DWORD dst_unused:UNUSED_PAD src0_sel:DWORD src1_sel:WORD_1
	ds_write_b64 v132, v[20:21] offset:4416
	v_mov_b32_e32 v20, v16
	v_mov_b32_e32 v21, v18
	v_pk_mul_f32 v[20:21], v[20:21], v[24:25] op_sel_hi:[1,0]
	v_mov_b32_e32 v18, v17
	v_pk_mul_f32 v[20:21], v[56:57], v[20:21]
	v_lshlrev_b32_e32 v23, 16, v153
	v_lshlrev_b32_e32 v22, 16, v152
	v_pk_mul_f32 v[16:17], v[18:19], v[24:25] op_sel_hi:[1,0]
	v_pk_mul_f32 v[20:21], v[20:21], v[22:23]
	v_pk_mul_f32 v[16:17], v[78:79], v[16:17]
	v_and_b32_e32 v19, 0xffff0000, v153
	v_and_b32_e32 v18, 0xffff0000, v152
	v_pk_mul_f32 v[16:17], v[16:17], v[18:19]
	v_and_b32_sdwa v18, v21, v213 dst_sel:DWORD dst_unused:UNUSED_PAD src0_sel:WORD_1 src1_sel:DWORD
	v_and_b32_sdwa v19, v20, v213 dst_sel:DWORD dst_unused:UNUSED_PAD src0_sel:WORD_1 src1_sel:DWORD
	v_add3_u32 v19, v20, v19, s76
	v_add3_u32 v18, v21, v18, s76
	v_and_b32_sdwa v20, v17, v213 dst_sel:DWORD dst_unused:UNUSED_PAD src0_sel:WORD_1 src1_sel:DWORD
	v_and_b32_sdwa v21, v16, v213 dst_sel:DWORD dst_unused:UNUSED_PAD src0_sel:WORD_1 src1_sel:DWORD
	v_add3_u32 v17, v17, v20, s76
	v_add3_u32 v16, v16, v21, s76
	v_and_b32_e32 v17, 0xffff0000, v17
	v_and_b32_e32 v16, 0xffff0000, v16
; __device__ __forceinline__ unsigned pk2(float lo, float hi) { return f2bf(lo) | (f2bf(hi) << 16); }
; __device__ __forceinline__ float rq_sum(float v) { v += __shfl_xor(v, 16); v += __shfl_xor(v, 32); return v; }
; __device__ __forceinline__ float frsq(float x) { return __builtin_amdgcn_rsqf(x); }
; __device__ __forceinline__ void ret_task(const Frame& F, int l, int task) {
;     ...
;     for (int qb = 0; qb < 2; ++qb) {
;         const int t = tq0 + qb * 16 + c;
;         float ss = 0.f;
; #pragma unroll
;         for (int eb = 0; eb < 8; ++eb) ss += (acc[qb][eb][0] * acc[qb][eb][0] + acc[qb][eb][1] * acc[qb][eb][1]) + (acc[qb][eb][2] * acc[qb][eb][2] + acc[qb][eb][3] * acc[qb][eb][3]);
;         const float rstd = frsq(rq_sum(ss) * (1.f / HD) + EPS);
; #pragma unroll
;         for (int eb = 0; eb < 8; ++eb) {
;             const int e0 = h * HD + eb * 16 + rq * 4;
;             const f32x4 gg = g4[eb]; const u32x2 gw = gwq[qb][eb];
;             u32x2 o; o.x = pk2(acc[qb][eb][0] * rstd * gg[0] * bf_lo(gw.x), acc[qb][eb][1] * rstd * gg[1] * bf_hi(gw.x));
;             o.y = pk2(acc[qb][eb][2] * rstd * gg[2] * bf_lo(gw.y), acc[qb][eb][3] * rstd * gg[3] * bf_hi(gw.y));
;             st_u2(MIX + (size_t)t * D + 1024 + e0, o);
;         }
	v_or_b32_sdwa v17, v17, v18 dst_sel:DWORD dst_unused:UNUSED_PAD src0_sel:DWORD src1_sel:WORD_1
	v_or_b32_sdwa v16, v16, v19 dst_sel:DWORD dst_unused:UNUSED_PAD src0_sel:DWORD src1_sel:WORD_1
	ds_write_b64 v132, v[16:17] offset:4448
	v_mov_b32_e32 v16, v12
	v_mov_b32_e32 v17, v14
	v_pk_mul_f32 v[16:17], v[16:17], v[24:25] op_sel_hi:[1,0]
	v_mov_b32_e32 v14, v13
	v_pk_mul_f32 v[16:17], v[76:77], v[16:17]
	v_lshlrev_b32_e32 v19, 16, v151
	v_lshlrev_b32_e32 v18, 16, v150
	v_pk_mul_f32 v[12:13], v[14:15], v[24:25] op_sel_hi:[1,0]
	v_pk_mul_f32 v[16:17], v[16:17], v[18:19]
	v_pk_mul_f32 v[12:13], v[74:75], v[12:13]
	v_and_b32_e32 v15, 0xffff0000, v151
	v_and_b32_e32 v14, 0xffff0000, v150
	v_pk_mul_f32 v[12:13], v[12:13], v[14:15]
	v_and_b32_sdwa v14, v17, v213 dst_sel:DWORD dst_unused:UNUSED_PAD src0_sel:WORD_1 src1_sel:DWORD
	v_and_b32_sdwa v15, v16, v213 dst_sel:DWORD dst_unused:UNUSED_PAD src0_sel:WORD_1 src1_sel:DWORD
	v_add3_u32 v15, v16, v15, s76
	v_add3_u32 v14, v17, v14, s76
	v_and_b32_sdwa v16, v13, v213 dst_sel:DWORD dst_unused:UNUSED_PAD src0_sel:WORD_1 src1_sel:DWORD
	v_and_b32_sdwa v17, v12, v213 dst_sel:DWORD dst_unused:UNUSED_PAD src0_sel:WORD_1 src1_sel:DWORD
	v_add3_u32 v13, v13, v16, s76
	v_add3_u32 v12, v12, v17, s76
	v_and_b32_e32 v13, 0xffff0000, v13
	v_and_b32_e32 v12, 0xffff0000, v12
	v_or_b32_sdwa v13, v13, v14 dst_sel:DWORD dst_unused:UNUSED_PAD src0_sel:DWORD src1_sel:WORD_1
	v_or_b32_sdwa v12, v12, v15 dst_sel:DWORD dst_unused:UNUSED_PAD src0_sel:DWORD src1_sel:WORD_1
	ds_write_b64 v132, v[12:13] offset:4480
	v_mov_b32_e32 v12, v8
	v_mov_b32_e32 v13, v10
	v_pk_mul_f32 v[12:13], v[12:13], v[24:25] op_sel_hi:[1,0]
	v_mov_b32_e32 v10, v9
	v_pk_mul_f32 v[12:13], v[68:69], v[12:13]
	v_lshlrev_b32_e32 v15, 16, v149
	v_lshlrev_b32_e32 v14, 16, v148
	v_pk_mul_f32 v[8:9], v[10:11], v[24:25] op_sel_hi:[1,0]
	v_pk_mul_f32 v[12:13], v[12:13], v[14:15]
	v_pk_mul_f32 v[8:9], v[66:67], v[8:9]
	v_and_b32_e32 v11, 0xffff0000, v149
	v_and_b32_e32 v10, 0xffff0000, v148
	v_pk_mul_f32 v[8:9], v[8:9], v[10:11]
	v_and_b32_sdwa v10, v13, v213 dst_sel:DWORD dst_unused:UNUSED_PAD src0_sel:WORD_1 src1_sel:DWORD
	v_and_b32_sdwa v11, v12, v213 dst_sel:DWORD dst_unused:UNUSED_PAD src0_sel:WORD_1 src1_sel:DWORD
	v_add3_u32 v11, v12, v11, s76
	v_add3_u32 v10, v13, v10, s76
	v_and_b32_sdwa v12, v9, v213 dst_sel:DWORD dst_unused:UNUSED_PAD src0_sel:WORD_1 src1_sel:DWORD
	v_and_b32_sdwa v13, v8, v213 dst_sel:DWORD dst_unused:UNUSED_PAD src0_sel:WORD_1 src1_sel:DWORD
	v_add3_u32 v9, v9, v12, s76
	v_add3_u32 v8, v8, v13, s76
	v_and_b32_e32 v9, 0xffff0000, v9
	v_and_b32_e32 v8, 0xffff0000, v8
	v_or_b32_sdwa v9, v9, v10 dst_sel:DWORD dst_unused:UNUSED_PAD src0_sel:DWORD src1_sel:WORD_1
	v_or_b32_sdwa v8, v8, v11 dst_sel:DWORD dst_unused:UNUSED_PAD src0_sel:DWORD src1_sel:WORD_1
	ds_write_b64 v132, v[8:9] offset:4512
	v_mov_b32_e32 v8, v4
	v_mov_b32_e32 v9, v6
	v_pk_mul_f32 v[8:9], v[8:9], v[24:25] op_sel_hi:[1,0]
	v_mov_b32_e32 v6, v5
	v_pk_mul_f32 v[8:9], v[48:49], v[8:9]
	v_lshlrev_b32_e32 v11, 16, v147
	v_lshlrev_b32_e32 v10, 16, v146
	v_pk_mul_f32 v[4:5], v[6:7], v[24:25] op_sel_hi:[1,0]
	v_pk_mul_f32 v[8:9], v[8:9], v[10:11]
	v_pk_mul_f32 v[4:5], v[54:55], v[4:5]
	v_and_b32_e32 v7, 0xffff0000, v147
	v_and_b32_e32 v6, 0xffff0000, v146
	v_pk_mul_f32 v[4:5], v[4:5], v[6:7]
	v_and_b32_sdwa v6, v9, v213 dst_sel:DWORD dst_unused:UNUSED_PAD src0_sel:WORD_1 src1_sel:DWORD
	v_and_b32_sdwa v7, v8, v213 dst_sel:DWORD dst_unused:UNUSED_PAD src0_sel:WORD_1 src1_sel:DWORD
	v_add3_u32 v7, v8, v7, s76
	v_add3_u32 v6, v9, v6, s76
	v_and_b32_sdwa v8, v5, v213 dst_sel:DWORD dst_unused:UNUSED_PAD src0_sel:WORD_1 src1_sel:DWORD
	v_and_b32_sdwa v9, v4, v213 dst_sel:DWORD dst_unused:UNUSED_PAD src0_sel:WORD_1 src1_sel:DWORD
	v_add3_u32 v5, v5, v8, s76
	v_add3_u32 v4, v4, v9, s76
	v_and_b32_e32 v5, 0xffff0000, v5
	v_and_b32_e32 v4, 0xffff0000, v4
	v_or_b32_sdwa v5, v5, v6 dst_sel:DWORD dst_unused:UNUSED_PAD src0_sel:DWORD src1_sel:WORD_1
	v_or_b32_sdwa v4, v4, v7 dst_sel:DWORD dst_unused:UNUSED_PAD src0_sel:DWORD src1_sel:WORD_1
	ds_write_b64 v132, v[4:5] offset:4544
	v_mov_b32_e32 v4, v0
	v_mov_b32_e32 v5, v2
	v_pk_mul_f32 v[4:5], v[4:5], v[24:25] op_sel_hi:[1,0]
	v_mov_b32_e32 v2, v1
	v_pk_mul_f32 v[4:5], v[44:45], v[4:5]
	v_lshlrev_b32_e32 v7, 16, v145
	v_lshlrev_b32_e32 v6, 16, v144
	v_pk_mul_f32 v[0:1], v[2:3], v[24:25] op_sel_hi:[1,0]
	v_pk_mul_f32 v[4:5], v[4:5], v[6:7]
	v_pk_mul_f32 v[0:1], v[26:27], v[0:1]
	v_and_b32_e32 v3, 0xffff0000, v145
	v_and_b32_e32 v2, 0xffff0000, v144
	v_pk_mul_f32 v[0:1], v[0:1], v[2:3]
	v_and_b32_sdwa v2, v5, v213 dst_sel:DWORD dst_unused:UNUSED_PAD src0_sel:WORD_1 src1_sel:DWORD
	v_and_b32_sdwa v3, v4, v213 dst_sel:DWORD dst_unused:UNUSED_PAD src0_sel:WORD_1 src1_sel:DWORD
	v_add3_u32 v3, v4, v3, s76
	v_add3_u32 v2, v5, v2, s76
	v_and_b32_sdwa v4, v1, v213 dst_sel:DWORD dst_unused:UNUSED_PAD src0_sel:WORD_1 src1_sel:DWORD
	v_and_b32_sdwa v5, v0, v213 dst_sel:DWORD dst_unused:UNUSED_PAD src0_sel:WORD_1 src1_sel:DWORD
	v_add3_u32 v1, v1, v4, s76
	v_add3_u32 v0, v0, v5, s76
	v_and_b32_e32 v1, 0xffff0000, v1
	v_and_b32_e32 v0, 0xffff0000, v0
	v_or_b32_sdwa v1, v1, v2 dst_sel:DWORD dst_unused:UNUSED_PAD src0_sel:DWORD src1_sel:WORD_1
	v_or_b32_sdwa v0, v0, v3 dst_sel:DWORD dst_unused:UNUSED_PAD src0_sel:DWORD src1_sel:WORD_1
	ds_write_b64 v132, v[0:1] offset:4576
	s_waitcnt lgkmcnt(0)
	ds_read_b128 v[168:171], v133
	ds_read_b128 v[172:175], v133 offset:1088
	ds_read_b128 v[176:179], v133 offset:2176
	ds_read_b128 v[180:183], v133 offset:3264
	ds_read_b128 v[112:115], v133 offset:4352
	ds_read_b128 v[116:119], v133 offset:5440
	ds_read_b128 v[120:123], v133 offset:6528
	ds_read_b128 v[124:127], v133 offset:7616
	v_mov_b32_e32 v136, 0x4000
	v_mov_b32_e32 v137, 0
	s_waitcnt lgkmcnt(7)
	global_store_dwordx4 v[130:131], v[168:171], off
	v_lshl_add_u64 v[130:131], v[130:131], 0, v[136:137]
	s_waitcnt lgkmcnt(6)
	global_store_dwordx4 v[130:131], v[172:175], off
	v_lshl_add_u64 v[130:131], v[130:131], 0, v[136:137]
	s_waitcnt lgkmcnt(5)
	global_store_dwordx4 v[130:131], v[176:179], off
	v_lshl_add_u64 v[130:131], v[130:131], 0, v[136:137]
	s_waitcnt lgkmcnt(4)
	global_store_dwordx4 v[130:131], v[180:183], off
	v_lshl_add_u64 v[130:131], v[130:131], 0, v[136:137]
	s_waitcnt lgkmcnt(3)
	global_store_dwordx4 v[130:131], v[112:115], off
	v_lshl_add_u64 v[130:131], v[130:131], 0, v[136:137]
	s_waitcnt lgkmcnt(2)
	global_store_dwordx4 v[130:131], v[116:119], off
	v_lshl_add_u64 v[130:131], v[130:131], 0, v[136:137]
	s_waitcnt lgkmcnt(1)
	global_store_dwordx4 v[130:131], v[120:123], off
	v_lshl_add_u64 v[130:131], v[130:131], 0, v[136:137]
	s_waitcnt lgkmcnt(0)
	global_store_dwordx4 v[130:131], v[124:127], off
	s_cbranch_scc1 .LBB0_659
